# rows phases: ctx-row gate loads hoisted ahead of the X stores, vmcnt waits recomputed from register dependences (5 phases)
# speedup vs baseline: 1.0330x; 1.0330x over previous
.LBB0_677:
	v_add_co_u32_e32 v18, vcc, 0xdd200000, v28
	s_cmpk_lt_i32 s6, 0x400
	s_nop 0
	v_addc_co_u32_e32 v19, vcc, -1, v29, vcc
	global_load_dwordx2 v[20:21], v[18:19], off offset:-1536
	global_load_dwordx2 v[34:35], v[18:19], off offset:-1024
	global_load_dwordx2 v[36:37], v[18:19], off offset:-512
	global_load_dwordx2 v[40:41], v[18:19], off
	s_cselect_b64 s[4:5], -1, 0
	s_cmpk_gt_i32 s6, 0x3ff
	s_waitcnt vmcnt(3)
	v_lshlrev_b32_e32 v30, 16, v20
	v_and_b32_e32 v31, 0xffff0000, v20
	v_lshlrev_b32_e32 v32, 16, v21
	v_and_b32_e32 v33, 0xffff0000, v21
	s_waitcnt vmcnt(2)
	v_lshlrev_b32_e32 v44, 16, v34
	v_and_b32_e32 v45, 0xffff0000, v34
	v_lshlrev_b32_e32 v34, 16, v35
	v_and_b32_e32 v35, 0xffff0000, v35
	s_waitcnt vmcnt(1)
	v_lshlrev_b32_e32 v42, 16, v36
	v_and_b32_e32 v43, 0xffff0000, v36
	v_lshlrev_b32_e32 v36, 16, v37
	v_and_b32_e32 v37, 0xffff0000, v37
	s_waitcnt vmcnt(0)
	v_lshlrev_b32_e32 v38, 16, v40
	v_and_b32_e32 v39, 0xffff0000, v40
	v_lshlrev_b32_e32 v40, 16, v41
	v_and_b32_e32 v41, 0xffff0000, v41
	s_cbranch_scc1 .LBB0_676
	v_add_co_u32_e32 v48, vcc, 0xff200000, v28
	v_lshl_add_u64 v[56:57], v[28:29], 0, s[14:15]
	s_nop 0
	v_addc_co_u32_e32 v49, vcc, -1, v29, vcc
	v_add_co_u32_e32 v52, vcc, s7, v28
	global_load_dwordx2 v[46:47], v[48:49], off offset:-1536
	s_nop 0
	v_addc_co_u32_e32 v53, vcc, -1, v29, vcc
	v_add_co_u32_e32 v62, vcc, s9, v28
	global_load_dwordx2 v[50:51], v[52:53], off offset:-1536
	s_nop 0
	v_addc_co_u32_e32 v63, vcc, -1, v29, vcc
	v_add_co_u32_e32 v76, vcc, s22, v28
	global_load_dwordx2 v[54:55], v[62:63], off offset:-1536
	s_nop 0
	v_addc_co_u32_e32 v77, vcc, -1, v29, vcc
	v_add_co_u32_e32 v78, vcc, s23, v28
	global_load_dwordx2 v[60:61], v[76:77], off offset:-1536
	s_nop 0
	v_addc_co_u32_e32 v79, vcc, -1, v29, vcc
	v_add_co_u32_e32 v70, vcc, s30, v28
	global_load_dwordx2 v[74:75], v[78:79], off offset:-1536
	s_nop 0
	v_addc_co_u32_e32 v71, vcc, -1, v29, vcc
	global_load_dwordx2 v[72:73], v[70:71], off offset:-1536
	v_add_co_u32_e32 v64, vcc, s31, v28
	s_nop 1
	v_addc_co_u32_e32 v65, vcc, -1, v29, vcc
	global_load_dwordx2 v[68:69], v[64:65], off offset:-1536
	global_load_dwordx2 v[58:59], v[28:29], off offset:-1536
	global_load_dwordx4 v[18:21], v[26:27], off
	global_load_dwordx2 v[66:67], v[48:49], off offset:-1024
	global_load_dwordx2 v[80:81], v[48:49], off offset:-512
	global_load_dwordx2 v[82:83], v[48:49], off
	global_load_dwordx2 v[96:97], v[52:53], off offset:-1024
	global_load_dwordx2 v[98:99], v[52:53], off offset:-512
	global_load_dwordx2 v[84:85], v[52:53], off
	global_load_dwordx2 v[100:101], v[62:63], off offset:-1024
	global_load_dwordx2 v[102:103], v[62:63], off offset:-512
	global_load_dwordx2 v[86:87], v[62:63], off
	global_load_dwordx2 v[104:105], v[76:77], off offset:-1024
	global_load_dwordx2 v[106:107], v[76:77], off offset:-512
	global_load_dwordx2 v[88:89], v[76:77], off
	global_load_dwordx2 v[108:109], v[78:79], off offset:-1024
	global_load_dwordx2 v[110:111], v[78:79], off offset:-512
	global_load_dwordx2 v[90:91], v[78:79], off
	s_waitcnt vmcnt(23)
	v_lshlrev_b32_e32 v48, 16, v46
	v_and_b32_e32 v49, 0xffff0000, v46
	v_lshlrev_b32_e32 v46, 16, v47
	v_and_b32_e32 v47, 0xffff0000, v47
	v_pk_add_f32 v[48:49], v[48:49], 0 op_sel_hi:[1,0]
	v_pk_add_f32 v[46:47], v[46:47], 0 op_sel_hi:[1,0]
	s_waitcnt vmcnt(22)
	v_lshlrev_b32_e32 v52, 16, v50
	v_and_b32_e32 v53, 0xffff0000, v50
	v_lshlrev_b32_e32 v50, 16, v51
	v_and_b32_e32 v51, 0xffff0000, v51
	v_pk_add_f32 v[46:47], v[46:47], v[50:51]
	v_pk_add_f32 v[48:49], v[48:49], v[52:53]
	s_waitcnt vmcnt(21)
	v_lshlrev_b32_e32 v50, 16, v54
	v_and_b32_e32 v51, 0xffff0000, v54
	v_lshlrev_b32_e32 v52, 16, v55
	v_and_b32_e32 v53, 0xffff0000, v55
	v_pk_add_f32 v[48:49], v[48:49], v[50:51]
	v_pk_add_f32 v[46:47], v[46:47], v[52:53]
	s_waitcnt vmcnt(20)
	v_lshlrev_b32_e32 v50, 16, v60
	v_and_b32_e32 v51, 0xffff0000, v60
	v_lshlrev_b32_e32 v52, 16, v61
	v_and_b32_e32 v53, 0xffff0000, v61
	v_pk_add_f32 v[46:47], v[46:47], v[52:53]
	v_pk_add_f32 v[48:49], v[48:49], v[50:51]
	s_waitcnt vmcnt(19)
	v_lshlrev_b32_e32 v50, 16, v74
	v_and_b32_e32 v51, 0xffff0000, v74
	v_lshlrev_b32_e32 v52, 16, v75
	v_and_b32_e32 v53, 0xffff0000, v75
	v_pk_add_f32 v[48:49], v[48:49], v[50:51]
	v_pk_add_f32 v[46:47], v[46:47], v[52:53]
	s_waitcnt vmcnt(18)
	v_lshlrev_b32_e32 v60, 16, v72
	v_and_b32_e32 v61, 0xffff0000, v72
	v_lshlrev_b32_e32 v62, 16, v73
	v_and_b32_e32 v63, 0xffff0000, v73
	global_load_dwordx2 v[50:51], v[70:71], off offset:-1024
	global_load_dwordx2 v[52:53], v[70:71], off offset:-512
	global_load_dwordx2 v[54:55], v[70:71], off
	v_pk_add_f32 v[46:47], v[46:47], v[62:63]
	v_pk_add_f32 v[48:49], v[48:49], v[60:61]
	global_load_dwordx2 v[60:61], v[64:65], off offset:-1024
	global_load_dwordx2 v[62:63], v[64:65], off offset:-512
	global_load_dwordx2 v[70:71], v[64:65], off
	s_waitcnt vmcnt(23)
	v_lshlrev_b32_e32 v64, 16, v68
	v_and_b32_e32 v65, 0xffff0000, v68
	v_lshlrev_b32_e32 v68, 16, v69
	v_and_b32_e32 v69, 0xffff0000, v69
	v_pk_add_f32 v[48:49], v[48:49], v[64:65]
	s_waitcnt vmcnt(22)
	v_lshlrev_b32_e32 v74, 16, v58
	v_and_b32_e32 v75, 0xffff0000, v58
	v_pk_add_f32 v[46:47], v[46:47], v[68:69]
	v_lshlrev_b32_e32 v58, 16, v59
	v_and_b32_e32 v59, 0xffff0000, v59
	v_pk_add_f32 v[48:49], v[48:49], v[74:75]
	v_pk_add_f32 v[46:47], v[46:47], v[58:59]
	s_waitcnt vmcnt(21)
	v_pk_fma_f32 v[18:19], v[48:49], v[18:19], v[30:31]
	v_pk_fma_f32 v[32:33], v[46:47], v[20:21], v[32:33]
	v_bfe_u32 v20, v18, 16, 1
	v_add3_u32 v30, v18, v20, s33
	v_bfe_u32 v18, v19, 16, 1
	v_and_b32_sdwa v20, v33, v95 dst_sel:DWORD dst_unused:UNUSED_PAD src0_sel:WORD_1 src1_sel:DWORD
	v_add3_u32 v18, v19, v18, s33
	v_bfe_u32 v19, v32, 16, 1
	v_add3_u32 v20, v33, v20, s33
	v_and_b32_e32 v31, 0xffff0000, v18
	v_add3_u32 v19, v32, v19, s33
	v_and_b32_e32 v33, 0xffff0000, v20
	v_or_b32_sdwa v18, v31, v30 dst_sel:DWORD dst_unused:UNUSED_PAD src0_sel:DWORD src1_sel:WORD_1
	v_or_b32_sdwa v19, v33, v19 dst_sel:DWORD dst_unused:UNUSED_PAD src0_sel:DWORD src1_sel:WORD_1
	global_load_dwordx2 v[64:65], v[28:29], off offset:-1024
	global_load_dwordx2 v[68:69], v[28:29], off offset:-512
	global_load_dwordx2 v[72:73], v[28:29], off
	s_waitcnt vmcnt(23)
	v_lshlrev_b32_e32 v48, 16, v66
	global_load_dwordx4 v[246:249], v[26:27], off offset:1024
	global_load_dwordx4 v[242:245], v[26:27], off offset:2048
	global_load_dwordx4 v[238:241], v[26:27], off offset:3072
	global_store_dwordx2 v[56:57], v[18:19], off
	v_and_b32_e32 v49, 0xffff0000, v66
	v_lshlrev_b32_e32 v56, 16, v67
	v_and_b32_e32 v57, 0xffff0000, v67
	v_pk_add_f32 v[56:57], v[56:57], 0 op_sel_hi:[1,0]
	v_pk_add_f32 v[48:49], v[48:49], 0 op_sel_hi:[1,0]
	s_waitcnt vmcnt(24)
	v_lshlrev_b32_e32 v58, 16, v96
	v_and_b32_e32 v59, 0xffff0000, v96
	v_lshlrev_b32_e32 v66, 16, v97
	v_and_b32_e32 v67, 0xffff0000, v97
	v_pk_add_f32 v[48:49], v[48:49], v[58:59]
	v_pk_add_f32 v[56:57], v[56:57], v[66:67]
	s_waitcnt vmcnt(21)
	v_lshlrev_b32_e32 v58, 16, v100
	v_and_b32_e32 v59, 0xffff0000, v100
	v_lshlrev_b32_e32 v66, 16, v101
	v_and_b32_e32 v67, 0xffff0000, v101
	v_pk_add_f32 v[56:57], v[56:57], v[66:67]
	v_pk_add_f32 v[48:49], v[48:49], v[58:59]
	s_waitcnt vmcnt(18)
	v_lshlrev_b32_e32 v58, 16, v104
	v_and_b32_e32 v59, 0xffff0000, v104
	v_lshlrev_b32_e32 v66, 16, v105
	v_and_b32_e32 v67, 0xffff0000, v105
	v_pk_add_f32 v[48:49], v[48:49], v[58:59]
	v_pk_add_f32 v[56:57], v[56:57], v[66:67]
	s_waitcnt vmcnt(15)
	v_lshlrev_b32_e32 v58, 16, v108
	v_and_b32_e32 v59, 0xffff0000, v108
	v_lshlrev_b32_e32 v66, 16, v109
	v_and_b32_e32 v67, 0xffff0000, v109
	v_pk_add_f32 v[56:57], v[56:57], v[66:67]
	v_pk_add_f32 v[48:49], v[48:49], v[58:59]
	v_lshl_add_u64 v[46:47], v[28:29], 0, s[16:17]
	v_and_b32_e32 v30, 0xffff0000, v30
	s_waitcnt vmcnt(12)
	v_lshlrev_b32_e32 v58, 16, v50
	v_and_b32_e32 v59, 0xffff0000, v50
	v_lshlrev_b32_e32 v50, 16, v51
	v_and_b32_e32 v51, 0xffff0000, v51
	v_pk_add_f32 v[48:49], v[48:49], v[58:59]
	v_pk_add_f32 v[50:51], v[56:57], v[50:51]
	s_waitcnt vmcnt(9)
	v_lshlrev_b32_e32 v56, 16, v60
	v_and_b32_e32 v57, 0xffff0000, v60
	v_pk_add_f32 v[48:49], v[48:49], v[56:57]
	v_lshlrev_b32_e32 v58, 16, v61
	v_and_b32_e32 v59, 0xffff0000, v61
	v_pk_add_f32 v[50:51], v[50:51], v[58:59]
	v_lshlrev_b32_e32 v60, 16, v98
	v_and_b32_e32 v61, 0xffff0000, v98
	s_waitcnt vmcnt(6)
	v_lshlrev_b32_e32 v56, 16, v64
	v_and_b32_e32 v57, 0xffff0000, v64
	v_pk_add_f32 v[48:49], v[48:49], v[56:57]
	v_lshlrev_b32_e32 v58, 16, v65
	v_and_b32_e32 v59, 0xffff0000, v65
	s_waitcnt vmcnt(3)
	v_pk_fma_f32 v[44:45], v[48:49], v[246:247], v[44:45]
	v_pk_add_f32 v[50:51], v[50:51], v[58:59]
	v_pk_fma_f32 v[34:35], v[50:51], v[248:249], v[34:35]
	v_and_b32_sdwa v20, v35, v95 dst_sel:DWORD dst_unused:UNUSED_PAD src0_sel:WORD_1 src1_sel:DWORD
	v_cvt_pk_bf16_f32 v18, v44, v45
	v_bfe_u32 v19, v34, 16, 1
	v_add3_u32 v20, v35, v20, s33
	v_add3_u32 v19, v34, v19, s33
	v_and_b32_e32 v35, 0xffff0000, v20
	v_or_b32_sdwa v19, v35, v19 dst_sel:DWORD dst_unused:UNUSED_PAD src0_sel:DWORD src1_sel:WORD_1
	global_store_dwordx2 v[46:47], v[18:19], off
	v_lshlrev_b32_e32 v56, 16, v80
	v_and_b32_e32 v57, 0xffff0000, v80
	v_lshlrev_b32_e32 v58, 16, v81
	v_and_b32_e32 v59, 0xffff0000, v81
	v_pk_add_f32 v[58:59], v[58:59], 0 op_sel_hi:[1,0]
	v_pk_add_f32 v[56:57], v[56:57], 0 op_sel_hi:[1,0]
	v_lshlrev_b32_e32 v64, 16, v99
	v_and_b32_e32 v65, 0xffff0000, v99
	v_pk_add_f32 v[56:57], v[56:57], v[60:61]
	v_pk_add_f32 v[58:59], v[58:59], v[64:65]
	v_lshlrev_b32_e32 v60, 16, v102
	v_and_b32_e32 v61, 0xffff0000, v102
	v_lshlrev_b32_e32 v64, 16, v103
	v_and_b32_e32 v65, 0xffff0000, v103
	v_pk_add_f32 v[58:59], v[58:59], v[64:65]
	v_pk_add_f32 v[56:57], v[56:57], v[60:61]
	v_lshlrev_b32_e32 v60, 16, v106
	v_and_b32_e32 v61, 0xffff0000, v106
	v_lshlrev_b32_e32 v64, 16, v107
	v_and_b32_e32 v65, 0xffff0000, v107
	v_pk_add_f32 v[56:57], v[56:57], v[60:61]
	v_pk_add_f32 v[58:59], v[58:59], v[64:65]
	v_lshlrev_b32_e32 v60, 16, v110
	v_and_b32_e32 v61, 0xffff0000, v110
	v_lshlrev_b32_e32 v64, 16, v111
	v_and_b32_e32 v65, 0xffff0000, v111
	v_pk_add_f32 v[58:59], v[58:59], v[64:65]
	v_pk_add_f32 v[56:57], v[56:57], v[60:61]
	v_lshlrev_b32_e32 v60, 16, v52
	v_and_b32_e32 v61, 0xffff0000, v52
	v_lshlrev_b32_e32 v52, 16, v53
	v_and_b32_e32 v53, 0xffff0000, v53
	v_pk_add_f32 v[56:57], v[56:57], v[60:61]
	v_pk_add_f32 v[52:53], v[58:59], v[52:53]
	v_lshlrev_b32_e32 v58, 16, v62
	v_and_b32_e32 v59, 0xffff0000, v62
	v_lshlrev_b32_e32 v60, 16, v63
	v_and_b32_e32 v61, 0xffff0000, v63
	v_lshlrev_b32_e32 v48, 16, v68
	v_and_b32_e32 v49, 0xffff0000, v68
	v_lshlrev_b32_e32 v50, 16, v69
	v_and_b32_e32 v51, 0xffff0000, v69
	v_pk_add_f32 v[52:53], v[52:53], v[60:61]
	v_pk_add_f32 v[56:57], v[56:57], v[58:59]
	v_pk_add_f32 v[50:51], v[52:53], v[50:51]
	v_pk_add_f32 v[48:49], v[56:57], v[48:49]
	v_lshl_add_u64 v[46:47], v[28:29], 0, s[18:19]
	v_lshlrev_b32_e32 v52, 16, v82
	v_and_b32_e32 v53, 0xffff0000, v82
	v_lshlrev_b32_e32 v56, 16, v83
	v_and_b32_e32 v57, 0xffff0000, v83
	v_pk_add_f32 v[56:57], v[56:57], 0 op_sel_hi:[1,0]
	v_pk_add_f32 v[52:53], v[52:53], 0 op_sel_hi:[1,0]
	v_lshlrev_b32_e32 v58, 16, v84
	v_and_b32_e32 v59, 0xffff0000, v84
	v_lshlrev_b32_e32 v60, 16, v85
	v_and_b32_e32 v61, 0xffff0000, v85
	v_pk_add_f32 v[52:53], v[52:53], v[58:59]
	v_pk_add_f32 v[56:57], v[56:57], v[60:61]
	v_lshlrev_b32_e32 v58, 16, v86
	v_and_b32_e32 v59, 0xffff0000, v86
	v_lshlrev_b32_e32 v60, 16, v87
	v_and_b32_e32 v61, 0xffff0000, v87
	v_pk_add_f32 v[56:57], v[56:57], v[60:61]
	v_pk_add_f32 v[52:53], v[52:53], v[58:59]
	v_lshlrev_b32_e32 v58, 16, v88
	v_and_b32_e32 v59, 0xffff0000, v88
	v_lshlrev_b32_e32 v60, 16, v89
	v_and_b32_e32 v61, 0xffff0000, v89
	v_pk_add_f32 v[52:53], v[52:53], v[58:59]
	v_pk_add_f32 v[56:57], v[56:57], v[60:61]
	v_lshlrev_b32_e32 v58, 16, v90
	v_and_b32_e32 v59, 0xffff0000, v90
	v_lshlrev_b32_e32 v60, 16, v91
	v_and_b32_e32 v61, 0xffff0000, v91
	v_pk_add_f32 v[56:57], v[56:57], v[60:61]
	v_pk_add_f32 v[52:53], v[52:53], v[58:59]
	v_lshlrev_b32_e32 v58, 16, v54
	v_and_b32_e32 v59, 0xffff0000, v54
	s_waitcnt vmcnt(3)
	v_pk_fma_f32 v[36:37], v[50:51], v[244:245], v[36:37]
	v_pk_fma_f32 v[42:43], v[48:49], v[242:243], v[42:43]
	v_and_b32_sdwa v21, v37, v95 dst_sel:DWORD dst_unused:UNUSED_PAD src0_sel:WORD_1 src1_sel:DWORD
	v_bfe_u32 v20, v36, 16, 1
	v_add3_u32 v21, v37, v21, s33
	v_add3_u32 v20, v36, v20, s33
	v_and_b32_e32 v37, 0xffff0000, v21
	v_cvt_pk_bf16_f32 v18, v42, v43
	v_or_b32_sdwa v19, v37, v20 dst_sel:DWORD dst_unused:UNUSED_PAD src0_sel:DWORD src1_sel:WORD_1
	global_store_dwordx2 v[46:47], v[18:19], off
	v_lshlrev_b32_e32 v54, 16, v55
	v_and_b32_e32 v55, 0xffff0000, v55
	v_pk_add_f32 v[52:53], v[52:53], v[58:59]
	v_pk_add_f32 v[54:55], v[56:57], v[54:55]
	v_lshlrev_b32_e32 v56, 16, v70
	v_and_b32_e32 v57, 0xffff0000, v70
	v_lshlrev_b32_e32 v58, 16, v71
	v_and_b32_e32 v59, 0xffff0000, v71
	v_lshlrev_b32_e32 v48, 16, v72
	v_and_b32_e32 v49, 0xffff0000, v72
	v_lshlrev_b32_e32 v50, 16, v73
	v_and_b32_e32 v51, 0xffff0000, v73
	v_pk_add_f32 v[54:55], v[54:55], v[58:59]
	v_pk_add_f32 v[52:53], v[52:53], v[56:57]
	v_pk_add_f32 v[50:51], v[54:55], v[50:51]
	v_pk_add_f32 v[48:49], v[52:53], v[48:49]
	v_and_b32_sdwa v52, v32, v95 dst_sel:DWORD dst_unused:UNUSED_PAD src0_sel:WORD_1 src1_sel:DWORD
	v_add3_u32 v32, v32, v52, s33
	v_and_b32_sdwa v52, v45, v95 dst_sel:DWORD dst_unused:UNUSED_PAD src0_sel:WORD_1 src1_sel:DWORD
	v_and_b32_sdwa v53, v44, v95 dst_sel:DWORD dst_unused:UNUSED_PAD src0_sel:WORD_1 src1_sel:DWORD
	v_and_b32_sdwa v54, v34, v95 dst_sel:DWORD dst_unused:UNUSED_PAD src0_sel:WORD_1 src1_sel:DWORD
	v_add3_u32 v45, v45, v52, s33
	v_add3_u32 v44, v44, v53, s33
	v_add3_u32 v34, v34, v54, s33
	v_and_b32_sdwa v52, v43, v95 dst_sel:DWORD dst_unused:UNUSED_PAD src0_sel:WORD_1 src1_sel:DWORD
	v_and_b32_sdwa v53, v42, v95 dst_sel:DWORD dst_unused:UNUSED_PAD src0_sel:WORD_1 src1_sel:DWORD
	v_and_b32_sdwa v54, v36, v95 dst_sel:DWORD dst_unused:UNUSED_PAD src0_sel:WORD_1 src1_sel:DWORD
	v_add3_u32 v43, v43, v52, s33
	v_add3_u32 v42, v42, v53, s33
	v_add3_u32 v36, v36, v54, s33
	v_lshl_add_u64 v[46:47], v[28:29], 0, s[20:21]
	v_and_b32_e32 v32, 0xffff0000, v32
	v_and_b32_e32 v45, 0xffff0000, v45
	v_and_b32_e32 v44, 0xffff0000, v44
	v_and_b32_e32 v34, 0xffff0000, v34
	v_and_b32_e32 v43, 0xffff0000, v43
	v_and_b32_e32 v42, 0xffff0000, v42
	v_and_b32_e32 v36, 0xffff0000, v36
	s_waitcnt vmcnt(3)
	v_pk_fma_f32 v[20:21], v[50:51], v[240:241], v[40:41]
	v_pk_fma_f32 v[18:19], v[48:49], v[238:239], v[38:39]
	v_and_b32_sdwa v49, v21, v95 dst_sel:DWORD dst_unused:UNUSED_PAD src0_sel:WORD_1 src1_sel:DWORD
	v_bfe_u32 v38, v18, 16, 1
	v_bfe_u32 v39, v19, 16, 1
	v_bfe_u32 v40, v20, 16, 1
	v_and_b32_sdwa v41, v19, v95 dst_sel:DWORD dst_unused:UNUSED_PAD src0_sel:WORD_1 src1_sel:DWORD
	v_and_b32_sdwa v48, v18, v95 dst_sel:DWORD dst_unused:UNUSED_PAD src0_sel:WORD_1 src1_sel:DWORD
	v_and_b32_sdwa v50, v20, v95 dst_sel:DWORD dst_unused:UNUSED_PAD src0_sel:WORD_1 src1_sel:DWORD
	v_add3_u32 v38, v18, v38, s33
	v_add3_u32 v21, v21, v49, s33
	v_add3_u32 v51, v19, v39, s33
	v_add3_u32 v52, v20, v40, s33
	v_add3_u32 v19, v19, v41, s33
	v_add3_u32 v18, v18, v48, s33
	v_add3_u32 v20, v20, v50, s33
	v_lshrrev_b32_e32 v40, 16, v38
	v_and_b32_e32 v41, 0xffff0000, v21
	v_and_b32_e32 v39, 0xffff0000, v19
	v_and_b32_e32 v38, 0xffff0000, v18
	v_and_or_b32 v18, v51, s3, v40
	v_and_b32_e32 v40, 0xffff0000, v20
	v_or_b32_sdwa v19, v41, v52 dst_sel:DWORD dst_unused:UNUSED_PAD src0_sel:DWORD src1_sel:WORD_1
	global_store_dwordx2 v[46:47], v[18:19], off
	s_branch .LBB0_676

.LBB0_892:
	v_add_co_u32_e32 v18, vcc, 0xdcc00000, v28
	s_cmpk_lt_i32 s6, 0x400
	s_nop 0
	v_addc_co_u32_e32 v19, vcc, -1, v29, vcc
	global_load_dwordx2 v[20:21], v[18:19], off offset:-1536
	global_load_dwordx2 v[34:35], v[18:19], off offset:-1024
	global_load_dwordx2 v[36:37], v[18:19], off offset:-512
	s_nop 0
	global_load_dwordx2 v[18:19], v[18:19], off
	s_cselect_b64 s[4:5], -1, 0
	s_cmpk_gt_i32 s6, 0x3ff
	s_waitcnt vmcnt(3)
	v_lshlrev_b32_e32 v30, 16, v20
	v_and_b32_e32 v31, 0xffff0000, v20
	v_lshlrev_b32_e32 v32, 16, v21
	v_and_b32_e32 v33, 0xffff0000, v21
	s_waitcnt vmcnt(2)
	v_lshlrev_b32_e32 v38, 16, v34
	v_and_b32_e32 v39, 0xffff0000, v34
	v_lshlrev_b32_e32 v34, 16, v35
	v_and_b32_e32 v35, 0xffff0000, v35
	s_waitcnt vmcnt(1)
	v_lshlrev_b32_e32 v44, 16, v36
	v_and_b32_e32 v45, 0xffff0000, v36
	v_lshlrev_b32_e32 v40, 16, v37
	v_and_b32_e32 v41, 0xffff0000, v37
	s_waitcnt vmcnt(0)
	v_lshlrev_b32_e32 v36, 16, v18
	v_and_b32_e32 v37, 0xffff0000, v18
	v_lshlrev_b32_e32 v42, 16, v19
	v_and_b32_e32 v43, 0xffff0000, v19
	s_cbranch_scc1 .LBB0_891
	v_add_co_u32_e32 v76, vcc, 0xfec00000, v28
	v_lshl_add_u64 v[46:47], v[28:29], 0, s[14:15]
	s_nop 0
	v_addc_co_u32_e32 v77, vcc, -1, v29, vcc
	v_add_co_u32_e32 v74, vcc, s7, v28
	global_load_dwordx2 v[50:51], v[76:77], off offset:-1536
	s_nop 0
	v_addc_co_u32_e32 v75, vcc, -1, v29, vcc
	v_add_co_u32_e32 v78, vcc, s9, v28
	global_load_dwordx2 v[48:49], v[28:29], off offset:-1536
	s_nop 0
	v_addc_co_u32_e32 v79, vcc, -1, v29, vcc
	v_add_co_u32_e32 v66, vcc, s22, v28
	global_load_dwordx2 v[72:73], v[78:79], off offset:-1536
	global_load_dwordx2 v[52:53], v[74:75], off offset:-1536
	v_addc_co_u32_e32 v67, vcc, -1, v29, vcc
	v_add_co_u32_e32 v62, vcc, s23, v28
	global_load_dwordx2 v[70:71], v[66:67], off offset:-1536
	s_nop 0
	v_addc_co_u32_e32 v63, vcc, -1, v29, vcc
	v_add_co_u32_e32 v56, vcc, s30, v28
	global_load_dwordx2 v[68:69], v[62:63], off offset:-1536
	s_nop 0
	v_addc_co_u32_e32 v57, vcc, -1, v29, vcc
	v_add_co_u32_e32 v54, vcc, s31, v28
	global_load_dwordx2 v[64:65], v[56:57], off offset:-1536
	s_nop 0
	v_addc_co_u32_e32 v55, vcc, -1, v29, vcc
	global_load_dwordx2 v[58:59], v[54:55], off offset:-1536
	v_add_co_u32_e32 v84, vcc, s33, v28
	s_waitcnt vmcnt(7)
	v_lshlrev_b32_e32 v106, 16, v50
	v_addc_co_u32_e32 v85, vcc, -1, v29, vcc
	global_load_dwordx2 v[86:87], v[84:85], off offset:-1536
	global_load_dwordx4 v[18:21], v[26:27], off
	v_add_co_u32_e32 v80, vcc, s35, v28
	v_and_b32_e32 v107, 0xffff0000, v50
	s_nop 0
	v_addc_co_u32_e32 v81, vcc, -1, v29, vcc
	global_load_dwordx2 v[82:83], v[80:81], off offset:-1536
	global_load_dwordx2 v[60:61], v[76:77], off offset:-1024
	global_load_dwordx2 v[88:89], v[76:77], off offset:-512
	s_nop 0
	global_load_dwordx2 v[76:77], v[76:77], off
	v_add_co_u32_e32 v98, vcc, s36, v28
	v_lshlrev_b32_e32 v50, 16, v51
	s_nop 0
	v_addc_co_u32_e32 v99, vcc, -1, v29, vcc
	global_load_dwordx2 v[100:101], v[98:99], off offset:-1536
	global_load_dwordx2 v[102:103], v[74:75], off offset:-1024
	global_load_dwordx2 v[90:91], v[74:75], off offset:-512
	s_nop 0
	global_load_dwordx2 v[74:75], v[74:75], off
	s_nop 0
	global_load_dwordx2 v[104:105], v[78:79], off offset:-1024
	global_load_dwordx2 v[92:93], v[78:79], off offset:-512
	s_nop 0
	global_load_dwordx2 v[78:79], v[78:79], off
	v_and_b32_e32 v51, 0xffff0000, v51
	v_pk_add_f32 v[50:51], v[50:51], 0 op_sel_hi:[1,0]
	v_pk_add_f32 v[106:107], v[106:107], 0 op_sel_hi:[1,0]
	s_waitcnt vmcnt(17)
	v_lshlrev_b32_e32 v108, 16, v52
	v_and_b32_e32 v109, 0xffff0000, v52
	v_lshlrev_b32_e32 v52, 16, v53
	v_and_b32_e32 v53, 0xffff0000, v53
	v_pk_add_f32 v[106:107], v[106:107], v[108:109]
	v_pk_add_f32 v[50:51], v[50:51], v[52:53]
	v_lshlrev_b32_e32 v52, 16, v72
	v_and_b32_e32 v53, 0xffff0000, v72
	v_lshlrev_b32_e32 v72, 16, v73
	v_and_b32_e32 v73, 0xffff0000, v73
	v_pk_add_f32 v[108:109], v[50:51], v[72:73]
	v_pk_add_f32 v[52:53], v[106:107], v[52:53]
	global_load_dwordx2 v[106:107], v[66:67], off offset:-1024
	global_load_dwordx2 v[72:73], v[66:67], off offset:-512
	global_load_dwordx2 v[50:51], v[66:67], off
	s_waitcnt vmcnt(19)
	v_lshlrev_b32_e32 v66, 16, v70
	v_and_b32_e32 v67, 0xffff0000, v70
	v_lshlrev_b32_e32 v70, 16, v71
	v_and_b32_e32 v71, 0xffff0000, v71
	v_pk_add_f32 v[66:67], v[52:53], v[66:67]
	v_pk_add_f32 v[108:109], v[108:109], v[70:71]
	global_load_dwordx2 v[110:111], v[62:63], off offset:-1024
	global_load_dwordx2 v[70:71], v[62:63], off offset:-512
	global_load_dwordx2 v[52:53], v[62:63], off
	s_waitcnt vmcnt(21)
	v_lshlrev_b32_e32 v62, 16, v68
	v_and_b32_e32 v63, 0xffff0000, v68
	v_lshlrev_b32_e32 v68, 16, v69
	v_and_b32_e32 v69, 0xffff0000, v69
	v_pk_add_f32 v[108:109], v[108:109], v[68:69]
	v_pk_add_f32 v[62:63], v[66:67], v[62:63]
	s_waitcnt vmcnt(20)
	v_lshlrev_b32_e32 v66, 16, v64
	v_and_b32_e32 v67, 0xffff0000, v64
	v_lshlrev_b32_e32 v64, 16, v65
	v_and_b32_e32 v65, 0xffff0000, v65
	v_pk_add_f32 v[62:63], v[62:63], v[66:67]
	v_pk_add_f32 v[64:65], v[108:109], v[64:65]
	s_waitcnt vmcnt(19)
	v_lshlrev_b32_e32 v66, 16, v58
	v_and_b32_e32 v67, 0xffff0000, v58
	v_lshlrev_b32_e32 v58, 16, v59
	v_and_b32_e32 v59, 0xffff0000, v59
	global_load_dwordx2 v[112:113], v[56:57], off offset:-1024
	global_load_dwordx2 v[68:69], v[56:57], off offset:-512
	s_nop 0
	global_load_dwordx2 v[56:57], v[56:57], off
	s_nop 0
	global_load_dwordx2 v[108:109], v[54:55], off offset:-1024
	global_load_dwordx2 v[114:115], v[54:55], off offset:-512
	s_nop 0
	global_load_dwordx2 v[54:55], v[54:55], off
	v_pk_add_f32 v[64:65], v[64:65], v[58:59]
	v_pk_add_f32 v[62:63], v[62:63], v[66:67]
	global_load_dwordx2 v[116:117], v[84:85], off offset:-1024
	global_load_dwordx2 v[118:119], v[84:85], off offset:-512
	global_load_dwordx2 v[58:59], v[84:85], off
	v_lshlrev_b32_e32 v124, 16, v48
	v_and_b32_e32 v125, 0xffff0000, v48
	v_lshlrev_b32_e32 v48, 16, v49
	v_and_b32_e32 v49, 0xffff0000, v49
	s_waitcnt vmcnt(27)
	v_lshlrev_b32_e32 v66, 16, v86
	v_and_b32_e32 v67, 0xffff0000, v86
	v_lshlrev_b32_e32 v84, 16, v87
	v_and_b32_e32 v85, 0xffff0000, v87
	v_pk_add_f32 v[66:67], v[62:63], v[66:67]
	v_pk_add_f32 v[64:65], v[64:65], v[84:85]
	global_load_dwordx2 v[84:85], v[80:81], off offset:-1024
	global_load_dwordx2 v[86:87], v[80:81], off offset:-512
	global_load_dwordx2 v[62:63], v[80:81], off
	s_waitcnt vmcnt(28)
	v_lshlrev_b32_e32 v80, 16, v82
	v_and_b32_e32 v81, 0xffff0000, v82
	v_lshlrev_b32_e32 v82, 16, v83
	v_and_b32_e32 v83, 0xffff0000, v83
	v_pk_add_f32 v[82:83], v[64:65], v[82:83]
	v_pk_add_f32 v[66:67], v[66:67], v[80:81]
	global_load_dwordx2 v[80:81], v[98:99], off offset:-1024
	global_load_dwordx2 v[120:121], v[98:99], off offset:-512
	global_load_dwordx2 v[64:65], v[98:99], off
	s_waitcnt vmcnt(27)
	v_lshlrev_b32_e32 v98, 16, v100
	v_and_b32_e32 v99, 0xffff0000, v100
	v_lshlrev_b32_e32 v100, 16, v101
	v_and_b32_e32 v101, 0xffff0000, v101
	v_pk_add_f32 v[98:99], v[66:67], v[98:99]
	v_pk_add_f32 v[82:83], v[82:83], v[100:101]
	global_load_dwordx2 v[100:101], v[28:29], off offset:-1024
	global_load_dwordx2 v[122:123], v[28:29], off offset:-512
	global_load_dwordx2 v[66:67], v[28:29], off
	v_pk_add_f32 v[48:49], v[82:83], v[48:49]
	v_pk_add_f32 v[82:83], v[98:99], v[124:125]
	v_pk_fma_f32 v[32:33], v[48:49], v[20:21], v[32:33]
	v_pk_fma_f32 v[18:19], v[82:83], v[18:19], v[30:31]
	v_lshlrev_b32_e32 v48, 16, v60
	v_bfe_u32 v20, v18, 16, 1
	v_add3_u32 v30, v18, v20, s37
	v_bfe_u32 v18, v19, 16, 1
	v_and_b32_sdwa v20, v33, v97 dst_sel:DWORD dst_unused:UNUSED_PAD src0_sel:WORD_1 src1_sel:DWORD
	v_add3_u32 v18, v19, v18, s37
	v_bfe_u32 v19, v32, 16, 1
	v_add3_u32 v20, v33, v20, s37
	v_and_b32_e32 v31, 0xffff0000, v18
	v_add3_u32 v19, v32, v19, s37
	v_and_b32_e32 v33, 0xffff0000, v20
	v_or_b32_sdwa v18, v31, v30 dst_sel:DWORD dst_unused:UNUSED_PAD src0_sel:DWORD src1_sel:WORD_1
	v_or_b32_sdwa v19, v33, v19 dst_sel:DWORD dst_unused:UNUSED_PAD src0_sel:DWORD src1_sel:WORD_1
	global_load_dwordx4 v[246:249], v[26:27], off offset:1024
	global_load_dwordx4 v[242:245], v[26:27], off offset:2048
	global_load_dwordx4 v[238:241], v[26:27], off offset:3072
	global_store_dwordx2 v[46:47], v[18:19], off
	v_and_b32_e32 v49, 0xffff0000, v60
	v_lshlrev_b32_e32 v60, 16, v61
	v_and_b32_e32 v61, 0xffff0000, v61
	v_pk_add_f32 v[48:49], v[48:49], 0 op_sel_hi:[1,0]
	v_pk_add_f32 v[60:61], v[60:61], 0 op_sel_hi:[1,0]
	s_waitcnt vmcnt(33)
	v_lshlrev_b32_e32 v82, 16, v102
	v_and_b32_e32 v83, 0xffff0000, v102
	v_lshlrev_b32_e32 v98, 16, v103
	v_and_b32_e32 v99, 0xffff0000, v103
	v_pk_add_f32 v[60:61], v[60:61], v[98:99]
	v_pk_add_f32 v[48:49], v[48:49], v[82:83]
	s_waitcnt vmcnt(30)
	v_lshlrev_b32_e32 v82, 16, v104
	v_and_b32_e32 v83, 0xffff0000, v104
	v_lshlrev_b32_e32 v98, 16, v105
	v_and_b32_e32 v99, 0xffff0000, v105
	v_pk_add_f32 v[48:49], v[48:49], v[82:83]
	v_pk_add_f32 v[60:61], v[60:61], v[98:99]
	s_waitcnt vmcnt(27)
	v_lshlrev_b32_e32 v82, 16, v106
	v_and_b32_e32 v83, 0xffff0000, v106
	v_lshlrev_b32_e32 v98, 16, v107
	v_and_b32_e32 v99, 0xffff0000, v107
	v_pk_add_f32 v[60:61], v[60:61], v[98:99]
	v_pk_add_f32 v[48:49], v[48:49], v[82:83]
	s_waitcnt vmcnt(24)
	v_lshlrev_b32_e32 v82, 16, v110
	v_and_b32_e32 v83, 0xffff0000, v110
	v_lshlrev_b32_e32 v98, 16, v111
	v_and_b32_e32 v99, 0xffff0000, v111
	v_pk_add_f32 v[48:49], v[48:49], v[82:83]
	v_pk_add_f32 v[60:61], v[60:61], v[98:99]
	s_waitcnt vmcnt(21)
	v_lshlrev_b32_e32 v82, 16, v112
	v_and_b32_e32 v83, 0xffff0000, v112
	v_lshlrev_b32_e32 v98, 16, v113
	v_and_b32_e32 v99, 0xffff0000, v113
	v_pk_add_f32 v[60:61], v[60:61], v[98:99]
	v_pk_add_f32 v[48:49], v[48:49], v[82:83]
	s_waitcnt vmcnt(18)
	v_lshlrev_b32_e32 v82, 16, v108
	v_and_b32_e32 v83, 0xffff0000, v108
	v_lshlrev_b32_e32 v98, 16, v109
	v_and_b32_e32 v99, 0xffff0000, v109
	v_pk_add_f32 v[48:49], v[48:49], v[82:83]
	v_pk_add_f32 v[60:61], v[60:61], v[98:99]
	s_waitcnt vmcnt(15)
	v_lshlrev_b32_e32 v82, 16, v116
	v_and_b32_e32 v83, 0xffff0000, v116
	v_lshlrev_b32_e32 v98, 16, v117
	v_and_b32_e32 v99, 0xffff0000, v117
	v_pk_add_f32 v[60:61], v[60:61], v[98:99]
	v_pk_add_f32 v[48:49], v[48:49], v[82:83]
	s_waitcnt vmcnt(12)
	v_lshlrev_b32_e32 v82, 16, v84
	v_and_b32_e32 v83, 0xffff0000, v84
	v_lshlrev_b32_e32 v84, 16, v85
	v_and_b32_e32 v85, 0xffff0000, v85
	v_pk_add_f32 v[48:49], v[48:49], v[82:83]
	v_pk_add_f32 v[60:61], v[60:61], v[84:85]
	s_waitcnt vmcnt(9)
	v_lshlrev_b32_e32 v82, 16, v80
	v_and_b32_e32 v83, 0xffff0000, v80
	v_lshlrev_b32_e32 v80, 16, v81
	v_and_b32_e32 v81, 0xffff0000, v81
	v_pk_add_f32 v[60:61], v[60:61], v[80:81]
	v_pk_add_f32 v[48:49], v[48:49], v[82:83]
	s_waitcnt vmcnt(6)
	v_lshlrev_b32_e32 v80, 16, v100
	v_and_b32_e32 v81, 0xffff0000, v100
	v_pk_add_f32 v[48:49], v[48:49], v[80:81]
	v_lshlrev_b32_e32 v82, 16, v101
	v_and_b32_e32 v83, 0xffff0000, v101
	v_pk_add_f32 v[60:61], v[60:61], v[82:83]
	v_lshl_add_u64 v[46:47], v[28:29], 0, s[16:17]
	v_lshlrev_b32_e32 v80, 16, v89
	v_and_b32_e32 v81, 0xffff0000, v89
	v_pk_add_f32 v[80:81], v[80:81], 0 op_sel_hi:[1,0]
	v_lshlrev_b32_e32 v82, 16, v90
	v_and_b32_e32 v83, 0xffff0000, v90
	v_lshlrev_b32_e32 v84, 16, v91
	v_and_b32_e32 v85, 0xffff0000, v91
	v_pk_add_f32 v[80:81], v[80:81], v[84:85]
	v_lshlrev_b32_e32 v84, 16, v93
	v_and_b32_e32 v85, 0xffff0000, v93
	v_pk_add_f32 v[80:81], v[80:81], v[84:85]
	v_and_b32_e32 v30, 0xffff0000, v30
	s_waitcnt vmcnt(3)
	v_pk_fma_f32 v[38:39], v[48:49], v[246:247], v[38:39]
	s_nop 0
	v_pk_fma_f32 v[34:35], v[60:61], v[248:249], v[34:35]
	v_and_b32_sdwa v20, v35, v97 dst_sel:DWORD dst_unused:UNUSED_PAD src0_sel:WORD_1 src1_sel:DWORD
	v_cvt_pk_bf16_f32 v18, v38, v39
	v_bfe_u32 v19, v34, 16, 1
	v_add3_u32 v20, v35, v20, s37
	v_add3_u32 v19, v34, v19, s37
	v_and_b32_e32 v35, 0xffff0000, v20
	v_or_b32_sdwa v19, v35, v19 dst_sel:DWORD dst_unused:UNUSED_PAD src0_sel:DWORD src1_sel:WORD_1
	global_store_dwordx2 v[46:47], v[18:19], off
	v_and_b32_sdwa v60, v32, v97 dst_sel:DWORD dst_unused:UNUSED_PAD src0_sel:WORD_1 src1_sel:DWORD
	v_add3_u32 v32, v32, v60, s37
	v_and_b32_sdwa v60, v39, v97 dst_sel:DWORD dst_unused:UNUSED_PAD src0_sel:WORD_1 src1_sel:DWORD
	v_and_b32_sdwa v61, v38, v97 dst_sel:DWORD dst_unused:UNUSED_PAD src0_sel:WORD_1 src1_sel:DWORD
	v_add3_u32 v39, v39, v60, s37
	v_add3_u32 v38, v38, v61, s37
	v_lshlrev_b32_e32 v60, 16, v88
	v_and_b32_e32 v61, 0xffff0000, v88
	v_pk_add_f32 v[60:61], v[60:61], 0 op_sel_hi:[1,0]
	v_lshl_add_u64 v[46:47], v[28:29], 0, s[18:19]
	v_pk_add_f32 v[60:61], v[60:61], v[82:83]
	v_lshlrev_b32_e32 v82, 16, v92
	v_and_b32_e32 v83, 0xffff0000, v92
	v_pk_add_f32 v[60:61], v[60:61], v[82:83]
	v_lshlrev_b32_e32 v82, 16, v72
	v_and_b32_e32 v83, 0xffff0000, v72
	v_lshlrev_b32_e32 v72, 16, v73
	v_and_b32_e32 v73, 0xffff0000, v73
	v_pk_add_f32 v[72:73], v[80:81], v[72:73]
	v_pk_add_f32 v[60:61], v[60:61], v[82:83]
	v_lshlrev_b32_e32 v80, 16, v70
	v_and_b32_e32 v81, 0xffff0000, v70
	v_lshlrev_b32_e32 v70, 16, v71
	v_and_b32_e32 v71, 0xffff0000, v71
	v_pk_add_f32 v[60:61], v[60:61], v[80:81]
	v_pk_add_f32 v[70:71], v[72:73], v[70:71]
	v_lshlrev_b32_e32 v72, 16, v68
	v_and_b32_e32 v73, 0xffff0000, v68
	v_lshlrev_b32_e32 v68, 16, v69
	v_and_b32_e32 v69, 0xffff0000, v69
	v_pk_add_f32 v[68:69], v[70:71], v[68:69]
	v_pk_add_f32 v[60:61], v[60:61], v[72:73]
	v_lshlrev_b32_e32 v70, 16, v114
	v_and_b32_e32 v71, 0xffff0000, v114
	v_pk_add_f32 v[60:61], v[60:61], v[70:71]
	v_lshlrev_b32_e32 v70, 16, v118
	v_and_b32_e32 v71, 0xffff0000, v118
	v_lshlrev_b32_e32 v72, 16, v115
	v_and_b32_e32 v73, 0xffff0000, v115
	v_pk_add_f32 v[60:61], v[60:61], v[70:71]
	v_lshlrev_b32_e32 v70, 16, v86
	v_and_b32_e32 v71, 0xffff0000, v86
	v_pk_add_f32 v[68:69], v[68:69], v[72:73]
	v_lshlrev_b32_e32 v72, 16, v119
	v_and_b32_e32 v73, 0xffff0000, v119
	v_pk_add_f32 v[60:61], v[60:61], v[70:71]
	v_lshlrev_b32_e32 v70, 16, v120
	v_and_b32_e32 v71, 0xffff0000, v120
	v_pk_add_f32 v[68:69], v[68:69], v[72:73]
	v_lshlrev_b32_e32 v72, 16, v87
	v_and_b32_e32 v73, 0xffff0000, v87
	v_pk_add_f32 v[60:61], v[60:61], v[70:71]
	v_lshlrev_b32_e32 v70, 16, v122
	v_and_b32_e32 v71, 0xffff0000, v122
	v_pk_add_f32 v[68:69], v[68:69], v[72:73]
	v_lshlrev_b32_e32 v72, 16, v121
	v_and_b32_e32 v73, 0xffff0000, v121
	v_pk_add_f32 v[60:61], v[60:61], v[70:71]
	v_pk_add_f32 v[68:69], v[68:69], v[72:73]
	v_lshlrev_b32_e32 v72, 16, v123
	v_and_b32_e32 v73, 0xffff0000, v123
	v_pk_add_f32 v[68:69], v[68:69], v[72:73]
	v_lshlrev_b32_e32 v70, 16, v75
	v_and_b32_e32 v71, 0xffff0000, v75
	v_lshl_add_u64 v[48:49], v[28:29], 0, s[20:21]
	v_and_b32_e32 v32, 0xffff0000, v32
	v_and_b32_e32 v39, 0xffff0000, v39
	v_and_b32_e32 v38, 0xffff0000, v38
	s_waitcnt vmcnt(3)
	v_pk_fma_f32 v[44:45], v[60:61], v[242:243], v[44:45]
	s_nop 0
	v_pk_fma_f32 v[40:41], v[68:69], v[244:245], v[40:41]
	v_and_b32_sdwa v20, v41, v97 dst_sel:DWORD dst_unused:UNUSED_PAD src0_sel:WORD_1 src1_sel:DWORD
	v_cvt_pk_bf16_f32 v18, v44, v45
	v_bfe_u32 v19, v40, 16, 1
	v_add3_u32 v20, v41, v20, s37
	v_add3_u32 v19, v40, v19, s37
	v_and_b32_e32 v41, 0xffff0000, v20
	v_or_b32_sdwa v19, v41, v19 dst_sel:DWORD dst_unused:UNUSED_PAD src0_sel:DWORD src1_sel:WORD_1
	global_store_dwordx2 v[46:47], v[18:19], off
	v_and_b32_sdwa v46, v34, v97 dst_sel:DWORD dst_unused:UNUSED_PAD src0_sel:WORD_1 src1_sel:DWORD
	v_add3_u32 v34, v34, v46, s37
	v_and_b32_sdwa v46, v45, v97 dst_sel:DWORD dst_unused:UNUSED_PAD src0_sel:WORD_1 src1_sel:DWORD
	v_and_b32_sdwa v47, v44, v97 dst_sel:DWORD dst_unused:UNUSED_PAD src0_sel:WORD_1 src1_sel:DWORD
	v_add3_u32 v45, v45, v46, s37
	v_add3_u32 v44, v44, v47, s37
	v_lshlrev_b32_e32 v46, 16, v76
	v_and_b32_e32 v47, 0xffff0000, v76
	v_lshlrev_b32_e32 v60, 16, v77
	v_and_b32_e32 v61, 0xffff0000, v77
	v_pk_add_f32 v[46:47], v[46:47], 0 op_sel_hi:[1,0]
	v_pk_add_f32 v[60:61], v[60:61], 0 op_sel_hi:[1,0]
	v_lshlrev_b32_e32 v68, 16, v74
	v_and_b32_e32 v69, 0xffff0000, v74
	v_pk_add_f32 v[60:61], v[60:61], v[70:71]
	v_pk_add_f32 v[46:47], v[46:47], v[68:69]
	v_lshlrev_b32_e32 v68, 16, v78
	v_and_b32_e32 v69, 0xffff0000, v78
	v_lshlrev_b32_e32 v70, 16, v79
	v_and_b32_e32 v71, 0xffff0000, v79
	v_pk_add_f32 v[46:47], v[46:47], v[68:69]
	v_pk_add_f32 v[60:61], v[60:61], v[70:71]
	v_lshlrev_b32_e32 v68, 16, v50
	v_and_b32_e32 v69, 0xffff0000, v50
	v_lshlrev_b32_e32 v50, 16, v51
	v_and_b32_e32 v51, 0xffff0000, v51
	v_pk_add_f32 v[50:51], v[60:61], v[50:51]
	v_pk_add_f32 v[46:47], v[46:47], v[68:69]
	v_lshlrev_b32_e32 v60, 16, v52
	v_and_b32_e32 v61, 0xffff0000, v52
	v_lshlrev_b32_e32 v52, 16, v53
	v_and_b32_e32 v53, 0xffff0000, v53
	v_pk_add_f32 v[46:47], v[46:47], v[60:61]
	v_pk_add_f32 v[50:51], v[50:51], v[52:53]
	v_lshlrev_b32_e32 v52, 16, v56
	v_and_b32_e32 v53, 0xffff0000, v56
	v_pk_add_f32 v[46:47], v[46:47], v[52:53]
	v_lshlrev_b32_e32 v52, 16, v54
	v_and_b32_e32 v53, 0xffff0000, v54
	v_pk_add_f32 v[46:47], v[46:47], v[52:53]
	v_lshlrev_b32_e32 v52, 16, v58
	v_and_b32_e32 v53, 0xffff0000, v58
	v_lshlrev_b32_e32 v56, 16, v57
	v_and_b32_e32 v57, 0xffff0000, v57
	v_pk_add_f32 v[46:47], v[46:47], v[52:53]
	v_lshlrev_b32_e32 v52, 16, v62
	v_and_b32_e32 v53, 0xffff0000, v62
	v_pk_add_f32 v[50:51], v[50:51], v[56:57]
	v_lshlrev_b32_e32 v54, 16, v55
	v_and_b32_e32 v55, 0xffff0000, v55
	v_pk_add_f32 v[46:47], v[46:47], v[52:53]
	v_lshlrev_b32_e32 v52, 16, v64
	v_and_b32_e32 v53, 0xffff0000, v64
	v_pk_add_f32 v[50:51], v[50:51], v[54:55]
	v_lshlrev_b32_e32 v54, 16, v59
	v_and_b32_e32 v55, 0xffff0000, v59
	v_pk_add_f32 v[46:47], v[46:47], v[52:53]
	v_lshlrev_b32_e32 v52, 16, v66
	v_and_b32_e32 v53, 0xffff0000, v66
	v_pk_add_f32 v[50:51], v[50:51], v[54:55]
	v_lshlrev_b32_e32 v54, 16, v63
	v_and_b32_e32 v55, 0xffff0000, v63
	v_pk_add_f32 v[46:47], v[46:47], v[52:53]
	v_pk_add_f32 v[50:51], v[50:51], v[54:55]
	v_lshlrev_b32_e32 v54, 16, v65
	v_and_b32_e32 v55, 0xffff0000, v65
	v_pk_add_f32 v[50:51], v[50:51], v[54:55]
	v_lshlrev_b32_e32 v54, 16, v67
	v_and_b32_e32 v55, 0xffff0000, v67
	v_pk_add_f32 v[50:51], v[50:51], v[54:55]
	v_and_b32_sdwa v52, v40, v97 dst_sel:DWORD dst_unused:UNUSED_PAD src0_sel:WORD_1 src1_sel:DWORD
	v_add3_u32 v40, v40, v52, s37
	v_and_b32_e32 v34, 0xffff0000, v34
	v_and_b32_e32 v45, 0xffff0000, v45
	v_and_b32_e32 v44, 0xffff0000, v44
	v_and_b32_e32 v40, 0xffff0000, v40
	s_waitcnt vmcnt(3)
	v_pk_fma_f32 v[18:19], v[46:47], v[238:239], v[36:37]
	s_nop 0
	v_pk_fma_f32 v[20:21], v[50:51], v[240:241], v[42:43]
	v_cvt_pk_bf16_f32 v46, v18, v19
	v_bfe_u32 v36, v20, 16, 1
	v_and_b32_sdwa v37, v18, v97 dst_sel:DWORD dst_unused:UNUSED_PAD src0_sel:WORD_1 src1_sel:DWORD
	v_add3_u32 v47, v20, v36, s37
	v_and_b32_sdwa v36, v19, v97 dst_sel:DWORD dst_unused:UNUSED_PAD src0_sel:WORD_1 src1_sel:DWORD
	v_add3_u32 v18, v18, v37, s37
	v_add3_u32 v19, v19, v36, s37
	v_and_b32_e32 v36, 0xffff0000, v18
	v_and_b32_sdwa v18, v21, v97 dst_sel:DWORD dst_unused:UNUSED_PAD src0_sel:WORD_1 src1_sel:DWORD
	v_and_b32_e32 v37, 0xffff0000, v19
	v_and_b32_sdwa v19, v20, v97 dst_sel:DWORD dst_unused:UNUSED_PAD src0_sel:WORD_1 src1_sel:DWORD
	v_add3_u32 v18, v21, v18, s37
	v_add3_u32 v19, v20, v19, s37
	v_and_b32_e32 v43, 0xffff0000, v18
	v_and_b32_e32 v42, 0xffff0000, v19
	v_or_b32_sdwa v47, v43, v47 dst_sel:DWORD dst_unused:UNUSED_PAD src0_sel:DWORD src1_sel:WORD_1
	global_store_dwordx2 v[48:49], v[46:47], off
	s_branch .LBB0_891

.LBB0_1337:
	v_add_co_u32_e32 v18, vcc, 0xdda00000, v52
	s_cmpk_lt_i32 s42, 0x400
	s_nop 0
	v_addc_co_u32_e32 v19, vcc, -1, v53, vcc
	s_waitcnt lgkmcnt(5)
	global_load_dwordx2 v[22:23], v[18:19], off offset:-1536
	s_waitcnt lgkmcnt(4)
	global_load_dwordx2 v[24:25], v[18:19], off offset:-1024
	s_waitcnt lgkmcnt(3)
	global_load_dwordx2 v[26:27], v[18:19], off offset:-512
	s_waitcnt lgkmcnt(2)
	global_load_dwordx2 v[28:29], v[18:19], off
	s_cselect_b64 s[8:9], -1, 0
	s_cmpk_gt_i32 s42, 0x3ff
	s_waitcnt vmcnt(3)
	v_lshlrev_b32_e32 v20, 16, v22
	v_and_b32_e32 v21, 0xffff0000, v22
	v_lshlrev_b32_e32 v22, 16, v23
	v_and_b32_e32 v23, 0xffff0000, v23
	s_waitcnt vmcnt(2)
	v_lshlrev_b32_e32 v56, 16, v24
	s_waitcnt lgkmcnt(0)
	v_and_b32_e32 v57, 0xffff0000, v24
	v_lshlrev_b32_e32 v24, 16, v25
	v_and_b32_e32 v25, 0xffff0000, v25
	s_waitcnt vmcnt(1)
	v_lshlrev_b32_e32 v54, 16, v26
	v_and_b32_e32 v55, 0xffff0000, v26
	v_lshlrev_b32_e32 v26, 16, v27
	v_and_b32_e32 v27, 0xffff0000, v27
	s_waitcnt vmcnt(0)
	v_lshlrev_b32_e32 v18, 16, v28
	v_and_b32_e32 v19, 0xffff0000, v28
	v_lshlrev_b32_e32 v28, 16, v29
	v_and_b32_e32 v29, 0xffff0000, v29
	s_cbranch_scc1 .LBB0_1339
	v_add_co_u32_e32 v58, vcc, 0xffa00000, v52
	global_load_dwordx2 v[64:65], v[52:53], off offset:-1536
	s_nop 0
	v_addc_co_u32_e32 v59, vcc, -1, v53, vcc
	v_add_co_u32_e32 v68, vcc, s33, v52
	global_load_dwordx2 v[66:67], v[58:59], off offset:-1536
	s_nop 0
	v_addc_co_u32_e32 v69, vcc, -1, v53, vcc
	global_load_dwordx2 v[76:77], v[68:69], off offset:-1536
	v_add_co_u32_e32 v78, vcc, s36, v52
	v_lshl_add_u64 v[82:83], v[52:53], 0, s[52:53]
	s_nop 0
	v_addc_co_u32_e32 v79, vcc, -1, v53, vcc
	global_load_dwordx2 v[80:81], v[78:79], off offset:-1536
	global_load_dwordx4 v[60:63], v[50:51], off
	global_load_dwordx2 v[84:85], v[52:53], off offset:-1024
	global_load_dwordx2 v[86:87], v[52:53], off offset:-512
	global_load_dwordx2 v[88:89], v[52:53], off
	global_load_dwordx2 v[90:91], v[58:59], off offset:-1024
	global_load_dwordx2 v[92:93], v[58:59], off offset:-512
	global_load_dwordx2 v[94:95], v[58:59], off
	global_load_dwordx2 v[96:97], v[68:69], off offset:-1024
	global_load_dwordx2 v[98:99], v[68:69], off offset:-512
	s_nop 0
	global_load_dwordx2 v[68:69], v[68:69], off
	s_nop 0
	global_load_dwordx2 v[100:101], v[78:79], off offset:-1024
	global_load_dwordx2 v[102:103], v[78:79], off offset:-512
	s_nop 0
	global_load_dwordx2 v[78:79], v[78:79], off
	s_waitcnt vmcnt(16)
	v_lshlrev_b32_e32 v58, 16, v64
	v_and_b32_e32 v59, 0xffff0000, v64
	v_lshlrev_b32_e32 v64, 16, v65
	v_and_b32_e32 v65, 0xffff0000, v65
	s_waitcnt vmcnt(15)
	v_lshlrev_b32_e32 v104, 16, v66
	v_and_b32_e32 v105, 0xffff0000, v66
	v_lshlrev_b32_e32 v66, 16, v67
	v_and_b32_e32 v67, 0xffff0000, v67
	v_pk_add_f32 v[104:105], v[104:105], 0 op_sel_hi:[1,0]
	v_pk_add_f32 v[66:67], v[66:67], 0 op_sel_hi:[1,0]
	s_waitcnt vmcnt(14)
	v_lshlrev_b32_e32 v106, 16, v76
	v_and_b32_e32 v107, 0xffff0000, v76
	v_lshlrev_b32_e32 v76, 16, v77
	v_and_b32_e32 v77, 0xffff0000, v77
	v_pk_add_f32 v[66:67], v[66:67], v[76:77]
	v_pk_add_f32 v[76:77], v[104:105], v[106:107]
	s_waitcnt vmcnt(13)
	v_lshlrev_b32_e32 v104, 16, v80
	v_and_b32_e32 v105, 0xffff0000, v80
	v_lshlrev_b32_e32 v80, 16, v81
	v_and_b32_e32 v81, 0xffff0000, v81
	v_pk_add_f32 v[76:77], v[76:77], v[104:105]
	v_pk_add_f32 v[66:67], v[66:67], v[80:81]
	v_pk_add_f32 v[58:59], v[76:77], v[58:59]
	v_pk_add_f32 v[64:65], v[66:67], v[64:65]
	s_waitcnt vmcnt(12)
	v_pk_fma_f32 v[20:21], v[58:59], v[60:61], v[20:21]
	v_pk_fma_f32 v[22:23], v[64:65], v[62:63], v[22:23]
	v_bfe_u32 v59, v21, 16, 1
	v_and_b32_sdwa v61, v23, v74 dst_sel:DWORD dst_unused:UNUSED_PAD src0_sel:WORD_1 src1_sel:DWORD
	v_bfe_u32 v58, v20, 16, 1
	v_bfe_u32 v60, v22, 16, 1
	v_add3_u32 v21, v21, v59, s37
	v_add3_u32 v23, v23, v61, s37
	v_add3_u32 v20, v20, v58, s37
	v_add3_u32 v59, v22, v60, s37
	v_and_b32_e32 v21, 0xffff0000, v21
	v_and_b32_e32 v23, 0xffff0000, v23
	v_or_b32_sdwa v58, v21, v20 dst_sel:DWORD dst_unused:UNUSED_PAD src0_sel:DWORD src1_sel:WORD_1
	v_or_b32_sdwa v59, v23, v59 dst_sel:DWORD dst_unused:UNUSED_PAD src0_sel:DWORD src1_sel:WORD_1
	global_load_dwordx4 v[246:249], v[50:51], off offset:1024
	global_load_dwordx4 v[242:245], v[50:51], off offset:2048
	global_load_dwordx4 v[238:241], v[50:51], off offset:3072
	global_store_dwordx2 v[82:83], v[58:59], off
	s_waitcnt vmcnt(12)
	v_lshlrev_b32_e32 v76, 16, v90
	v_and_b32_e32 v77, 0xffff0000, v90
	v_lshlrev_b32_e32 v80, 16, v91
	v_and_b32_e32 v81, 0xffff0000, v91
	v_lshlrev_b32_e32 v64, 16, v84
	v_and_b32_e32 v65, 0xffff0000, v84
	v_lshlrev_b32_e32 v66, 16, v85
	v_and_b32_e32 v67, 0xffff0000, v85
	v_pk_add_f32 v[80:81], v[80:81], 0 op_sel_hi:[1,0]
	v_pk_add_f32 v[76:77], v[76:77], 0 op_sel_hi:[1,0]
	s_waitcnt vmcnt(9)
	v_lshlrev_b32_e32 v82, 16, v96
	v_and_b32_e32 v83, 0xffff0000, v96
	v_lshlrev_b32_e32 v84, 16, v97
	v_and_b32_e32 v85, 0xffff0000, v97
	v_pk_add_f32 v[76:77], v[76:77], v[82:83]
	v_pk_add_f32 v[80:81], v[80:81], v[84:85]
	s_waitcnt vmcnt(6)
	v_lshlrev_b32_e32 v82, 16, v100
	v_and_b32_e32 v83, 0xffff0000, v100
	v_lshlrev_b32_e32 v84, 16, v101
	v_and_b32_e32 v85, 0xffff0000, v101
	v_pk_add_f32 v[80:81], v[80:81], v[84:85]
	v_pk_add_f32 v[76:77], v[76:77], v[82:83]
	v_pk_add_f32 v[66:67], v[80:81], v[66:67]
	v_pk_add_f32 v[64:65], v[76:77], v[64:65]
	v_lshl_add_u64 v[62:63], v[52:53], 0, s[54:55]
	v_lshlrev_b32_e32 v76, 16, v92
	v_and_b32_e32 v77, 0xffff0000, v92
	v_lshlrev_b32_e32 v80, 16, v93
	v_and_b32_e32 v81, 0xffff0000, v93
	v_pk_add_f32 v[80:81], v[80:81], 0 op_sel_hi:[1,0]
	v_pk_add_f32 v[76:77], v[76:77], 0 op_sel_hi:[1,0]
	v_lshlrev_b32_e32 v82, 16, v98
	v_and_b32_e32 v83, 0xffff0000, v98
	v_lshlrev_b32_e32 v84, 16, v99
	v_and_b32_e32 v85, 0xffff0000, v99
	v_pk_add_f32 v[76:77], v[76:77], v[82:83]
	v_pk_add_f32 v[80:81], v[80:81], v[84:85]
	s_waitcnt vmcnt(5)
	v_lshlrev_b32_e32 v82, 16, v102
	v_and_b32_e32 v83, 0xffff0000, v102
	v_lshlrev_b32_e32 v84, 16, v103
	v_and_b32_e32 v85, 0xffff0000, v103
	v_pk_add_f32 v[80:81], v[80:81], v[84:85]
	v_pk_add_f32 v[76:77], v[76:77], v[82:83]
	v_lshlrev_b32_e32 v82, 16, v68
	v_and_b32_e32 v83, 0xffff0000, v68
	v_lshlrev_b32_e32 v68, 16, v69
	v_and_b32_e32 v69, 0xffff0000, v69
	v_and_b32_e32 v20, 0xffff0000, v20
	s_waitcnt vmcnt(3)
	v_pk_fma_f32 v[24:25], v[66:67], v[248:249], v[24:25]
	v_pk_fma_f32 v[64:65], v[64:65], v[246:247], v[56:57]
	v_and_b32_sdwa v59, v25, v74 dst_sel:DWORD dst_unused:UNUSED_PAD src0_sel:WORD_1 src1_sel:DWORD
	v_bfe_u32 v58, v24, 16, 1
	v_add3_u32 v25, v25, v59, s37
	v_add3_u32 v58, v24, v58, s37
	v_and_b32_e32 v25, 0xffff0000, v25
	v_cvt_pk_bf16_f32 v56, v64, v65
	v_or_b32_sdwa v57, v25, v58 dst_sel:DWORD dst_unused:UNUSED_PAD src0_sel:DWORD src1_sel:WORD_1
	global_store_dwordx2 v[62:63], v[56:57], off
	v_lshlrev_b32_e32 v62, 16, v86
	v_and_b32_e32 v63, 0xffff0000, v86
	v_lshlrev_b32_e32 v66, 16, v87
	v_and_b32_e32 v67, 0xffff0000, v87
	v_pk_add_f32 v[62:63], v[76:77], v[62:63]
	v_pk_add_f32 v[66:67], v[80:81], v[66:67]
	v_lshl_add_u64 v[60:61], v[52:53], 0, s[56:57]
	v_lshlrev_b32_e32 v76, 16, v94
	v_and_b32_e32 v77, 0xffff0000, v94
	v_lshlrev_b32_e32 v80, 16, v95
	v_and_b32_e32 v81, 0xffff0000, v95
	v_pk_add_f32 v[80:81], v[80:81], 0 op_sel_hi:[1,0]
	v_pk_add_f32 v[76:77], v[76:77], 0 op_sel_hi:[1,0]
	v_pk_add_f32 v[68:69], v[80:81], v[68:69]
	v_pk_add_f32 v[76:77], v[76:77], v[82:83]
	v_lshlrev_b32_e32 v80, 16, v78
	v_and_b32_e32 v81, 0xffff0000, v78
	v_lshlrev_b32_e32 v78, 16, v79
	v_and_b32_e32 v79, 0xffff0000, v79
	v_pk_add_f32 v[76:77], v[76:77], v[80:81]
	v_pk_add_f32 v[68:69], v[68:69], v[78:79]
	s_waitcnt vmcnt(3)
	v_pk_fma_f32 v[26:27], v[66:67], v[244:245], v[26:27]
	v_pk_fma_f32 v[54:55], v[62:63], v[242:243], v[54:55]
	v_and_b32_sdwa v59, v27, v74 dst_sel:DWORD dst_unused:UNUSED_PAD src0_sel:WORD_1 src1_sel:DWORD
	v_bfe_u32 v58, v26, 16, 1
	v_add3_u32 v27, v27, v59, s37
	v_add3_u32 v58, v26, v58, s37
	v_and_b32_e32 v27, 0xffff0000, v27
	v_cvt_pk_bf16_f32 v56, v54, v55
	v_or_b32_sdwa v57, v27, v58 dst_sel:DWORD dst_unused:UNUSED_PAD src0_sel:DWORD src1_sel:WORD_1
	global_store_dwordx2 v[60:61], v[56:57], off
	v_lshlrev_b32_e32 v56, 16, v88
	v_and_b32_e32 v57, 0xffff0000, v88
	v_lshlrev_b32_e32 v66, 16, v89
	v_and_b32_e32 v67, 0xffff0000, v89
	v_pk_add_f32 v[76:77], v[76:77], v[56:57]
	v_and_b32_sdwa v56, v22, v74 dst_sel:DWORD dst_unused:UNUSED_PAD src0_sel:WORD_1 src1_sel:DWORD
	v_pk_add_f32 v[66:67], v[68:69], v[66:67]
	v_add3_u32 v22, v22, v56, s37
	v_and_b32_sdwa v56, v65, v74 dst_sel:DWORD dst_unused:UNUSED_PAD src0_sel:WORD_1 src1_sel:DWORD
	v_and_b32_sdwa v57, v64, v74 dst_sel:DWORD dst_unused:UNUSED_PAD src0_sel:WORD_1 src1_sel:DWORD
	v_add3_u32 v56, v65, v56, s37
	v_add3_u32 v64, v64, v57, s37
	v_and_b32_sdwa v65, v54, v74 dst_sel:DWORD dst_unused:UNUSED_PAD src0_sel:WORD_1 src1_sel:DWORD
	v_and_b32_sdwa v68, v24, v74 dst_sel:DWORD dst_unused:UNUSED_PAD src0_sel:WORD_1 src1_sel:DWORD
	v_and_b32_e32 v57, 0xffff0000, v56
	v_and_b32_e32 v56, 0xffff0000, v64
	v_and_b32_sdwa v64, v55, v74 dst_sel:DWORD dst_unused:UNUSED_PAD src0_sel:WORD_1 src1_sel:DWORD
	v_add3_u32 v54, v54, v65, s37
	v_add3_u32 v24, v24, v68, s37
	v_and_b32_sdwa v68, v26, v74 dst_sel:DWORD dst_unused:UNUSED_PAD src0_sel:WORD_1 src1_sel:DWORD
	v_add3_u32 v55, v55, v64, s37
	v_add3_u32 v26, v26, v68, s37
	v_lshl_add_u64 v[62:63], v[52:53], 0, s[58:59]
	v_and_b32_e32 v22, 0xffff0000, v22
	v_and_b32_e32 v24, 0xffff0000, v24
	v_and_b32_e32 v55, 0xffff0000, v55
	v_and_b32_e32 v54, 0xffff0000, v54
	v_and_b32_e32 v26, 0xffff0000, v26
	s_waitcnt vmcnt(3)
	v_pk_fma_f32 v[28:29], v[66:67], v[240:241], v[28:29]
	v_pk_fma_f32 v[18:19], v[76:77], v[238:239], v[18:19]
	v_and_b32_sdwa v65, v29, v74 dst_sel:DWORD dst_unused:UNUSED_PAD src0_sel:WORD_1 src1_sel:DWORD
	v_bfe_u32 v58, v18, 16, 1
	v_bfe_u32 v59, v19, 16, 1
	v_bfe_u32 v60, v28, 16, 1
	v_and_b32_sdwa v61, v19, v74 dst_sel:DWORD dst_unused:UNUSED_PAD src0_sel:WORD_1 src1_sel:DWORD
	v_and_b32_sdwa v64, v18, v74 dst_sel:DWORD dst_unused:UNUSED_PAD src0_sel:WORD_1 src1_sel:DWORD
	v_and_b32_sdwa v66, v28, v74 dst_sel:DWORD dst_unused:UNUSED_PAD src0_sel:WORD_1 src1_sel:DWORD
	v_add3_u32 v58, v18, v58, s37
	v_add3_u32 v29, v29, v65, s37
	v_add3_u32 v59, v19, v59, s37
	v_add3_u32 v60, v28, v60, s37
	v_add3_u32 v19, v19, v61, s37
	v_add3_u32 v18, v18, v64, s37
	v_add3_u32 v28, v28, v66, s37
	v_lshrrev_b32_e32 v58, 16, v58
	v_and_b32_e32 v29, 0xffff0000, v29
	v_and_b32_e32 v19, 0xffff0000, v19
	v_and_b32_e32 v18, 0xffff0000, v18
	v_and_b32_e32 v28, 0xffff0000, v28
	v_and_or_b32 v58, v59, s31, v58
	v_or_b32_sdwa v59, v29, v60 dst_sel:DWORD dst_unused:UNUSED_PAD src0_sel:DWORD src1_sel:WORD_1
	global_store_dwordx2 v[62:63], v[58:59], off

.LBB0_2017:
	v_add_co_u32_e32 v26, vcc, 0xdca00000, v24
	s_cmpk_lt_i32 s6, 0x400
	s_nop 0
	v_addc_co_u32_e32 v27, vcc, -1, v25, vcc
	global_load_dwordx2 v[28:29], v[26:27], off offset:-1536
	global_load_dwordx2 v[30:31], v[26:27], off offset:-1024
	global_load_dwordx2 v[34:35], v[26:27], off offset:-512
	global_load_dwordx2 v[38:39], v[26:27], off
	s_cselect_b64 s[4:5], -1, 0
	s_cmpk_gt_i32 s6, 0x3ff
	s_waitcnt vmcnt(3)
	v_lshlrev_b32_e32 v26, 16, v28
	v_and_b32_e32 v27, 0xffff0000, v28
	v_lshlrev_b32_e32 v28, 16, v29
	v_and_b32_e32 v29, 0xffff0000, v29
	s_waitcnt vmcnt(2)
	v_lshlrev_b32_e32 v32, 16, v30
	v_and_b32_e32 v33, 0xffff0000, v30
	v_lshlrev_b32_e32 v30, 16, v31
	v_and_b32_e32 v31, 0xffff0000, v31
	s_waitcnt vmcnt(1)
	v_lshlrev_b32_e32 v40, 16, v34
	v_and_b32_e32 v41, 0xffff0000, v34
	v_lshlrev_b32_e32 v36, 16, v35
	v_and_b32_e32 v37, 0xffff0000, v35
	s_waitcnt vmcnt(0)
	v_lshlrev_b32_e32 v34, 16, v38
	v_and_b32_e32 v35, 0xffff0000, v38
	v_lshlrev_b32_e32 v38, 16, v39
	v_and_b32_e32 v39, 0xffff0000, v39
	s_cbranch_scc1 .LBB0_2016
	v_add_co_u32_e32 v68, vcc, 0xfea00000, v24
	v_lshl_add_u64 v[42:43], v[24:25], 0, s[14:15]
	s_nop 0
	v_addc_co_u32_e32 v69, vcc, -1, v25, vcc
	v_add_co_u32_e32 v66, vcc, s7, v24
	global_load_dwordx2 v[46:47], v[68:69], off offset:-1536
	s_nop 0
	v_addc_co_u32_e32 v67, vcc, -1, v25, vcc
	global_load_dwordx2 v[64:65], v[66:67], off offset:-1536
	v_add_co_u32_e32 v60, vcc, s9, v24
	s_waitcnt vmcnt(1)
	v_lshlrev_b32_e32 v74, 16, v46
	v_addc_co_u32_e32 v61, vcc, -1, v25, vcc
	global_load_dwordx2 v[62:63], v[60:61], off offset:-1536
	v_add_co_u32_e32 v54, vcc, s22, v24
	v_and_b32_e32 v75, 0xffff0000, v46
	s_nop 0
	v_addc_co_u32_e32 v55, vcc, -1, v25, vcc
	v_add_co_u32_e32 v50, vcc, s23, v24
	global_load_dwordx2 v[58:59], v[54:55], off offset:-1536
	s_nop 0
	v_addc_co_u32_e32 v51, vcc, -1, v25, vcc
	v_add_co_u32_e32 v48, vcc, s30, v24
	global_load_dwordx2 v[56:57], v[50:51], off offset:-1536
	s_nop 0
	v_addc_co_u32_e32 v49, vcc, -1, v25, vcc
	v_add_co_u32_e32 v76, vcc, s31, v24
	global_load_dwordx2 v[52:53], v[48:49], off offset:-1536
	global_load_dwordx2 v[44:45], v[68:69], off offset:-1024
	global_load_dwordx2 v[70:71], v[68:69], off offset:-512
	s_nop 0
	global_load_dwordx2 v[68:69], v[68:69], off
	v_addc_co_u32_e32 v77, vcc, -1, v25, vcc
	v_add_co_u32_e32 v96, vcc, s33, v24
	global_load_dwordx2 v[86:87], v[76:77], off offset:-1536
	global_load_dwordx2 v[84:85], v[66:67], off offset:-1024
	global_load_dwordx2 v[72:73], v[66:67], off offset:-512
	s_nop 0
	global_load_dwordx2 v[66:67], v[66:67], off
	v_addc_co_u32_e32 v97, vcc, -1, v25, vcc
	v_add_co_u32_e32 v100, vcc, s36, v24
	global_load_dwordx2 v[98:99], v[96:97], off offset:-1536
	s_nop 0
	v_addc_co_u32_e32 v101, vcc, -1, v25, vcc
	v_add_co_u32_e32 v102, vcc, s37, v24
	global_load_dwordx2 v[104:105], v[100:101], off offset:-1536
	s_nop 0
	v_addc_co_u32_e32 v103, vcc, -1, v25, vcc
	v_add_co_u32_e32 v106, vcc, s40, v24
	global_load_dwordx2 v[108:109], v[102:103], off offset:-1536
	s_nop 0
	v_addc_co_u32_e32 v107, vcc, -1, v25, vcc
	v_lshlrev_b32_e32 v46, 16, v47
	v_and_b32_e32 v47, 0xffff0000, v47
	global_load_dwordx2 v[110:111], v[106:107], off offset:-1536
	v_pk_add_f32 v[46:47], v[46:47], 0 op_sel_hi:[1,0]
	s_waitcnt vmcnt(15)
	v_lshlrev_b32_e32 v78, 16, v64
	v_and_b32_e32 v79, 0xffff0000, v64
	v_lshlrev_b32_e32 v64, 16, v65
	v_and_b32_e32 v65, 0xffff0000, v65
	v_pk_add_f32 v[80:81], v[46:47], v[64:65]
	global_load_dwordx2 v[112:113], v[60:61], off offset:-1024
	global_load_dwordx2 v[64:65], v[60:61], off offset:-512
	global_load_dwordx2 v[46:47], v[60:61], off
	global_load_dwordx2 v[114:115], v[24:25], off offset:-1536
	v_pk_add_f32 v[74:75], v[74:75], 0 op_sel_hi:[1,0]
	s_waitcnt vmcnt(18)
	v_lshlrev_b32_e32 v60, 16, v62
	v_pk_add_f32 v[74:75], v[74:75], v[78:79]
	v_and_b32_e32 v61, 0xffff0000, v62
	v_pk_add_f32 v[60:61], v[74:75], v[60:61]
	global_load_dwordx4 v[92:95], v[22:23], off
	global_load_dwordx2 v[116:117], v[54:55], off offset:-1024
	global_load_dwordx2 v[74:75], v[54:55], off offset:-512
	s_nop 0
	global_load_dwordx2 v[54:55], v[54:55], off
	v_lshlrev_b32_e32 v62, 16, v63
	v_and_b32_e32 v63, 0xffff0000, v63
	v_pk_add_f32 v[62:63], v[80:81], v[62:63]
	s_waitcnt vmcnt(21)
	v_lshlrev_b32_e32 v78, 16, v58
	v_and_b32_e32 v79, 0xffff0000, v58
	v_lshlrev_b32_e32 v58, 16, v59
	v_and_b32_e32 v59, 0xffff0000, v59
	v_pk_add_f32 v[58:59], v[62:63], v[58:59]
	v_pk_add_f32 v[60:61], v[60:61], v[78:79]
	s_waitcnt vmcnt(20)
	v_lshlrev_b32_e32 v62, 16, v56
	v_and_b32_e32 v63, 0xffff0000, v56
	v_lshlrev_b32_e32 v56, 16, v57
	v_and_b32_e32 v57, 0xffff0000, v57
	v_pk_add_f32 v[60:61], v[60:61], v[62:63]
	v_pk_add_f32 v[56:57], v[58:59], v[56:57]
	s_waitcnt vmcnt(19)
	v_lshlrev_b32_e32 v58, 16, v52
	v_and_b32_e32 v59, 0xffff0000, v52
	v_lshlrev_b32_e32 v52, 16, v53
	v_and_b32_e32 v53, 0xffff0000, v53
	v_pk_add_f32 v[56:57], v[56:57], v[52:53]
	v_pk_add_f32 v[58:59], v[60:61], v[58:59]
	s_waitcnt vmcnt(15)
	v_lshlrev_b32_e32 v60, 16, v86
	v_and_b32_e32 v61, 0xffff0000, v86
	v_lshlrev_b32_e32 v62, 16, v87
	v_and_b32_e32 v63, 0xffff0000, v87
	global_load_dwordx2 v[118:119], v[50:51], off offset:-1024
	global_load_dwordx2 v[78:79], v[50:51], off offset:-512
	s_nop 0
	global_load_dwordx2 v[50:51], v[50:51], off
	s_nop 0
	global_load_dwordx2 v[120:121], v[48:49], off offset:-1024
	global_load_dwordx2 v[80:81], v[48:49], off offset:-512
	s_nop 0
	global_load_dwordx2 v[48:49], v[48:49], off
	s_nop 0
	global_load_dwordx2 v[122:123], v[76:77], off offset:-1024
	global_load_dwordx2 v[82:83], v[76:77], off offset:-512
	global_load_dwordx2 v[52:53], v[76:77], off
	v_pk_add_f32 v[58:59], v[58:59], v[60:61]
	v_pk_add_f32 v[60:61], v[56:57], v[62:63]
	s_waitcnt vmcnt(20)
	v_lshlrev_b32_e32 v62, 16, v98
	v_and_b32_e32 v63, 0xffff0000, v98
	v_lshlrev_b32_e32 v76, 16, v99
	v_and_b32_e32 v77, 0xffff0000, v99
	global_load_dwordx2 v[124:125], v[96:97], off offset:-1024
	global_load_dwordx2 v[86:87], v[96:97], off offset:-512
	global_load_dwordx2 v[56:57], v[96:97], off
	v_pk_add_f32 v[60:61], v[60:61], v[76:77]
	v_pk_add_f32 v[62:63], v[58:59], v[62:63]
	global_load_dwordx2 v[96:97], v[100:101], off offset:-1024
	global_load_dwordx2 v[98:99], v[100:101], off offset:-512
	global_load_dwordx2 v[58:59], v[100:101], off
	s_waitcnt vmcnt(25)
	v_lshlrev_b32_e32 v76, 16, v104
	v_and_b32_e32 v77, 0xffff0000, v104
	v_lshlrev_b32_e32 v100, 16, v105
	v_and_b32_e32 v101, 0xffff0000, v105
	v_pk_add_f32 v[62:63], v[62:63], v[76:77]
	v_pk_add_f32 v[76:77], v[60:61], v[100:101]
	global_load_dwordx2 v[100:101], v[102:103], off offset:-1024
	global_load_dwordx2 v[104:105], v[102:103], off offset:-512
	global_load_dwordx2 v[60:61], v[102:103], off
	s_waitcnt vmcnt(27)
	v_lshlrev_b32_e32 v102, 16, v108
	v_and_b32_e32 v103, 0xffff0000, v108
	v_lshlrev_b32_e32 v108, 16, v109
	v_and_b32_e32 v109, 0xffff0000, v109
	v_pk_add_f32 v[76:77], v[76:77], v[108:109]
	v_pk_add_f32 v[102:103], v[62:63], v[102:103]
	global_load_dwordx2 v[108:109], v[106:107], off offset:-1024
	global_load_dwordx2 v[126:127], v[106:107], off offset:-512
	global_load_dwordx2 v[62:63], v[106:107], off
	s_waitcnt vmcnt(29)
	v_lshlrev_b32_e32 v106, 16, v110
	v_and_b32_e32 v107, 0xffff0000, v110
	v_lshlrev_b32_e32 v110, 16, v111
	v_and_b32_e32 v111, 0xffff0000, v111
	v_pk_add_f32 v[102:103], v[102:103], v[106:107]
	s_waitcnt vmcnt(25)
	v_lshlrev_b32_e32 v130, 16, v114
	v_and_b32_e32 v131, 0xffff0000, v114
	v_pk_add_f32 v[106:107], v[76:77], v[110:111]
	v_lshlrev_b32_e32 v114, 16, v115
	v_and_b32_e32 v115, 0xffff0000, v115
	v_pk_add_f32 v[102:103], v[102:103], v[130:131]
	v_pk_add_f32 v[106:107], v[106:107], v[114:115]
	global_load_dwordx2 v[110:111], v[24:25], off offset:-1024
	global_load_dwordx2 v[128:129], v[24:25], off offset:-512
	global_load_dwordx2 v[76:77], v[24:25], off
	v_lshlrev_b32_e32 v114, 16, v44
	v_and_b32_e32 v115, 0xffff0000, v44
	v_lshlrev_b32_e32 v44, 16, v45
	v_and_b32_e32 v45, 0xffff0000, v45
	v_pk_add_f32 v[44:45], v[44:45], 0 op_sel_hi:[1,0]
	v_pk_add_f32 v[114:115], v[114:115], 0 op_sel_hi:[1,0]
	v_lshlrev_b32_e32 v130, 16, v84
	v_and_b32_e32 v131, 0xffff0000, v84
	v_lshlrev_b32_e32 v84, 16, v85
	v_and_b32_e32 v85, 0xffff0000, v85
	v_pk_add_f32 v[114:115], v[114:115], v[130:131]
	s_waitcnt vmcnt(27)
	v_pk_fma_f32 v[26:27], v[102:103], v[92:93], v[26:27]
	v_pk_fma_f32 v[28:29], v[106:107], v[94:95], v[28:29]
	v_bfe_u32 v92, v26, 16, 1
	v_add3_u32 v26, v26, v92, s41
	v_bfe_u32 v92, v27, 16, 1
	v_and_b32_sdwa v94, v29, v91 dst_sel:DWORD dst_unused:UNUSED_PAD src0_sel:WORD_1 src1_sel:DWORD
	v_add3_u32 v27, v27, v92, s41
	v_bfe_u32 v93, v28, 16, 1
	v_add3_u32 v29, v29, v94, s41
	v_and_b32_e32 v27, 0xffff0000, v27
	v_add3_u32 v93, v28, v93, s41
	v_and_b32_e32 v29, 0xffff0000, v29
	v_or_b32_sdwa v92, v27, v26 dst_sel:DWORD dst_unused:UNUSED_PAD src0_sel:DWORD src1_sel:WORD_1
	v_or_b32_sdwa v93, v29, v93 dst_sel:DWORD dst_unused:UNUSED_PAD src0_sel:DWORD src1_sel:WORD_1
	global_load_dwordx4 v[246:249], v[22:23], off offset:1024
	global_load_dwordx4 v[242:245], v[22:23], off offset:2048
	global_load_dwordx4 v[238:241], v[22:23], off offset:3072
	global_store_dwordx2 v[42:43], v[92:93], off
	v_pk_add_f32 v[44:45], v[44:45], v[84:85]
	v_lshlrev_b32_e32 v84, 16, v112
	v_and_b32_e32 v85, 0xffff0000, v112
	v_lshlrev_b32_e32 v112, 16, v113
	v_and_b32_e32 v113, 0xffff0000, v113
	v_pk_add_f32 v[44:45], v[44:45], v[112:113]
	v_pk_add_f32 v[84:85], v[114:115], v[84:85]
	s_waitcnt vmcnt(30)
	v_lshlrev_b32_e32 v112, 16, v116
	v_and_b32_e32 v113, 0xffff0000, v116
	v_lshlrev_b32_e32 v114, 16, v117
	v_and_b32_e32 v115, 0xffff0000, v117
	v_pk_add_f32 v[84:85], v[84:85], v[112:113]
	v_pk_add_f32 v[44:45], v[44:45], v[114:115]
	s_waitcnt vmcnt(27)
	v_lshlrev_b32_e32 v112, 16, v118
	v_and_b32_e32 v113, 0xffff0000, v118
	v_lshlrev_b32_e32 v114, 16, v119
	v_and_b32_e32 v115, 0xffff0000, v119
	v_pk_add_f32 v[44:45], v[44:45], v[114:115]
	v_pk_add_f32 v[84:85], v[84:85], v[112:113]
	s_waitcnt vmcnt(24)
	v_lshlrev_b32_e32 v112, 16, v120
	v_and_b32_e32 v113, 0xffff0000, v120
	v_lshlrev_b32_e32 v114, 16, v121
	v_and_b32_e32 v115, 0xffff0000, v121
	v_pk_add_f32 v[84:85], v[84:85], v[112:113]
	v_pk_add_f32 v[44:45], v[44:45], v[114:115]
	s_waitcnt vmcnt(21)
	v_lshlrev_b32_e32 v112, 16, v122
	v_and_b32_e32 v113, 0xffff0000, v122
	v_lshlrev_b32_e32 v114, 16, v123
	v_and_b32_e32 v115, 0xffff0000, v123
	v_pk_add_f32 v[44:45], v[44:45], v[114:115]
	v_pk_add_f32 v[84:85], v[84:85], v[112:113]
	s_waitcnt vmcnt(18)
	v_lshlrev_b32_e32 v112, 16, v124
	v_and_b32_e32 v113, 0xffff0000, v124
	v_lshlrev_b32_e32 v114, 16, v125
	v_and_b32_e32 v115, 0xffff0000, v125
	v_pk_add_f32 v[84:85], v[84:85], v[112:113]
	v_pk_add_f32 v[44:45], v[44:45], v[114:115]
	s_waitcnt vmcnt(15)
	v_lshlrev_b32_e32 v112, 16, v96
	v_and_b32_e32 v113, 0xffff0000, v96
	v_lshlrev_b32_e32 v96, 16, v97
	v_and_b32_e32 v97, 0xffff0000, v97
	v_pk_add_f32 v[44:45], v[44:45], v[96:97]
	v_pk_add_f32 v[84:85], v[84:85], v[112:113]
	s_waitcnt vmcnt(12)
	v_lshlrev_b32_e32 v96, 16, v100
	v_and_b32_e32 v97, 0xffff0000, v100
	v_lshlrev_b32_e32 v100, 16, v101
	v_and_b32_e32 v101, 0xffff0000, v101
	v_pk_add_f32 v[84:85], v[84:85], v[96:97]
	s_waitcnt vmcnt(9)
	v_lshlrev_b32_e32 v96, 16, v108
	v_and_b32_e32 v97, 0xffff0000, v108
	v_pk_add_f32 v[44:45], v[44:45], v[100:101]
	v_lshlrev_b32_e32 v100, 16, v109
	v_and_b32_e32 v101, 0xffff0000, v109
	v_pk_add_f32 v[84:85], v[84:85], v[96:97]
	s_waitcnt vmcnt(6)
	v_lshlrev_b32_e32 v96, 16, v110
	v_and_b32_e32 v97, 0xffff0000, v110
	v_pk_add_f32 v[44:45], v[44:45], v[100:101]
	v_lshlrev_b32_e32 v100, 16, v111
	v_and_b32_e32 v101, 0xffff0000, v111
	v_pk_add_f32 v[84:85], v[84:85], v[96:97]
	v_pk_add_f32 v[44:45], v[44:45], v[100:101]
	v_lshl_add_u64 v[102:103], v[24:25], 0, s[16:17]
	v_lshl_add_u64 v[106:107], v[24:25], 0, s[18:19]
	v_and_b32_sdwa v96, v28, v91 dst_sel:DWORD dst_unused:UNUSED_PAD src0_sel:WORD_1 src1_sel:DWORD
	v_add3_u32 v28, v28, v96, s41
	v_lshl_add_u64 v[42:43], v[24:25], 0, s[20:21]
	v_and_b32_e32 v26, 0xffff0000, v26
	v_and_b32_e32 v28, 0xffff0000, v28
	s_waitcnt vmcnt(3)
	v_pk_fma_f32 v[32:33], v[84:85], v[246:247], v[32:33]
	v_pk_fma_f32 v[30:31], v[44:45], v[248:249], v[30:31]
	v_and_b32_sdwa v92, v31, v91 dst_sel:DWORD dst_unused:UNUSED_PAD src0_sel:WORD_1 src1_sel:DWORD
	v_cvt_pk_bf16_f32 v44, v32, v33
	v_bfe_u32 v45, v30, 16, 1
	v_add3_u32 v31, v31, v92, s41
	v_add3_u32 v45, v30, v45, s41
	v_and_b32_e32 v31, 0xffff0000, v31
	v_or_b32_sdwa v45, v31, v45 dst_sel:DWORD dst_unused:UNUSED_PAD src0_sel:DWORD src1_sel:WORD_1
	global_store_dwordx2 v[102:103], v[44:45], off
	v_and_b32_sdwa v84, v33, v91 dst_sel:DWORD dst_unused:UNUSED_PAD src0_sel:WORD_1 src1_sel:DWORD
	v_and_b32_sdwa v85, v32, v91 dst_sel:DWORD dst_unused:UNUSED_PAD src0_sel:WORD_1 src1_sel:DWORD
	v_lshlrev_b32_e32 v44, 16, v70
	v_and_b32_e32 v45, 0xffff0000, v70
	v_lshlrev_b32_e32 v70, 16, v71
	v_and_b32_e32 v71, 0xffff0000, v71
	v_add3_u32 v33, v33, v84, s41
	v_add3_u32 v32, v32, v85, s41
	v_pk_add_f32 v[70:71], v[70:71], 0 op_sel_hi:[1,0]
	v_pk_add_f32 v[44:45], v[44:45], 0 op_sel_hi:[1,0]
	v_lshlrev_b32_e32 v84, 16, v72
	v_and_b32_e32 v85, 0xffff0000, v72
	v_lshlrev_b32_e32 v72, 16, v73
	v_and_b32_e32 v73, 0xffff0000, v73
	v_pk_add_f32 v[44:45], v[44:45], v[84:85]
	v_pk_add_f32 v[70:71], v[70:71], v[72:73]
	v_lshlrev_b32_e32 v72, 16, v64
	v_and_b32_e32 v73, 0xffff0000, v64
	v_lshlrev_b32_e32 v64, 16, v65
	v_and_b32_e32 v65, 0xffff0000, v65
	v_pk_add_f32 v[64:65], v[70:71], v[64:65]
	v_pk_add_f32 v[44:45], v[44:45], v[72:73]
	v_lshlrev_b32_e32 v70, 16, v74
	v_and_b32_e32 v71, 0xffff0000, v74
	v_pk_add_f32 v[44:45], v[44:45], v[70:71]
	v_lshlrev_b32_e32 v70, 16, v78
	v_and_b32_e32 v71, 0xffff0000, v78
	v_lshlrev_b32_e32 v72, 16, v75
	v_and_b32_e32 v73, 0xffff0000, v75
	v_pk_add_f32 v[44:45], v[44:45], v[70:71]
	v_lshlrev_b32_e32 v70, 16, v80
	v_and_b32_e32 v71, 0xffff0000, v80
	v_pk_add_f32 v[64:65], v[64:65], v[72:73]
	v_lshlrev_b32_e32 v72, 16, v79
	v_and_b32_e32 v73, 0xffff0000, v79
	v_pk_add_f32 v[44:45], v[44:45], v[70:71]
	v_lshlrev_b32_e32 v70, 16, v82
	v_and_b32_e32 v71, 0xffff0000, v82
	v_pk_add_f32 v[64:65], v[64:65], v[72:73]
	v_lshlrev_b32_e32 v72, 16, v81
	v_and_b32_e32 v73, 0xffff0000, v81
	v_pk_add_f32 v[44:45], v[44:45], v[70:71]
	v_lshlrev_b32_e32 v70, 16, v86
	v_and_b32_e32 v71, 0xffff0000, v86
	v_pk_add_f32 v[64:65], v[64:65], v[72:73]
	v_lshlrev_b32_e32 v72, 16, v83
	v_and_b32_e32 v73, 0xffff0000, v83
	v_pk_add_f32 v[44:45], v[44:45], v[70:71]
	v_lshlrev_b32_e32 v70, 16, v98
	v_and_b32_e32 v71, 0xffff0000, v98
	v_pk_add_f32 v[64:65], v[64:65], v[72:73]
	v_lshlrev_b32_e32 v72, 16, v87
	v_and_b32_e32 v73, 0xffff0000, v87
	v_pk_add_f32 v[44:45], v[44:45], v[70:71]
	v_lshlrev_b32_e32 v70, 16, v104
	v_and_b32_e32 v71, 0xffff0000, v104
	v_pk_add_f32 v[64:65], v[64:65], v[72:73]
	v_lshlrev_b32_e32 v72, 16, v99
	v_and_b32_e32 v73, 0xffff0000, v99
	v_pk_add_f32 v[44:45], v[44:45], v[70:71]
	v_lshlrev_b32_e32 v70, 16, v126
	v_and_b32_e32 v71, 0xffff0000, v126
	v_pk_add_f32 v[64:65], v[64:65], v[72:73]
	v_lshlrev_b32_e32 v72, 16, v105
	v_and_b32_e32 v73, 0xffff0000, v105
	v_pk_add_f32 v[44:45], v[44:45], v[70:71]
	v_lshlrev_b32_e32 v70, 16, v128
	v_and_b32_e32 v71, 0xffff0000, v128
	v_pk_add_f32 v[64:65], v[64:65], v[72:73]
	v_lshlrev_b32_e32 v72, 16, v127
	v_and_b32_e32 v73, 0xffff0000, v127
	v_pk_add_f32 v[44:45], v[44:45], v[70:71]
	v_pk_add_f32 v[64:65], v[64:65], v[72:73]
	v_lshlrev_b32_e32 v72, 16, v129
	v_and_b32_e32 v73, 0xffff0000, v129
	v_pk_add_f32 v[64:65], v[64:65], v[72:73]
	v_and_b32_sdwa v70, v30, v91 dst_sel:DWORD dst_unused:UNUSED_PAD src0_sel:WORD_1 src1_sel:DWORD
	v_add3_u32 v30, v30, v70, s41
	v_and_b32_e32 v33, 0xffff0000, v33
	s_waitcnt vmcnt(3)
	v_pk_fma_f32 v[40:41], v[44:45], v[242:243], v[40:41]
	v_pk_fma_f32 v[36:37], v[64:65], v[244:245], v[36:37]
	v_and_b32_sdwa v70, v37, v91 dst_sel:DWORD dst_unused:UNUSED_PAD src0_sel:WORD_1 src1_sel:DWORD
	v_cvt_pk_bf16_f32 v44, v40, v41
	v_bfe_u32 v45, v36, 16, 1
	v_add3_u32 v37, v37, v70, s41
	v_add3_u32 v45, v36, v45, s41
	v_and_b32_e32 v37, 0xffff0000, v37
	v_or_b32_sdwa v45, v37, v45 dst_sel:DWORD dst_unused:UNUSED_PAD src0_sel:DWORD src1_sel:WORD_1
	global_store_dwordx2 v[106:107], v[44:45], off
	v_and_b32_sdwa v64, v41, v91 dst_sel:DWORD dst_unused:UNUSED_PAD src0_sel:WORD_1 src1_sel:DWORD
	v_and_b32_sdwa v65, v40, v91 dst_sel:DWORD dst_unused:UNUSED_PAD src0_sel:WORD_1 src1_sel:DWORD
	v_add3_u32 v41, v41, v64, s41
	v_add3_u32 v40, v40, v65, s41
	v_lshlrev_b32_e32 v44, 16, v68
	v_and_b32_e32 v45, 0xffff0000, v68
	v_lshlrev_b32_e32 v64, 16, v69
	v_and_b32_e32 v65, 0xffff0000, v69
	v_pk_add_f32 v[64:65], v[64:65], 0 op_sel_hi:[1,0]
	v_pk_add_f32 v[44:45], v[44:45], 0 op_sel_hi:[1,0]
	v_lshlrev_b32_e32 v68, 16, v66
	v_and_b32_e32 v69, 0xffff0000, v66
	v_lshlrev_b32_e32 v66, 16, v67
	v_and_b32_e32 v67, 0xffff0000, v67
	v_pk_add_f32 v[44:45], v[44:45], v[68:69]
	v_pk_add_f32 v[64:65], v[64:65], v[66:67]
	v_lshlrev_b32_e32 v66, 16, v46
	v_and_b32_e32 v67, 0xffff0000, v46
	v_lshlrev_b32_e32 v46, 16, v47
	v_and_b32_e32 v47, 0xffff0000, v47
	v_pk_add_f32 v[46:47], v[64:65], v[46:47]
	v_pk_add_f32 v[44:45], v[44:45], v[66:67]
	v_lshlrev_b32_e32 v64, 16, v54
	v_and_b32_e32 v65, 0xffff0000, v54
	v_lshlrev_b32_e32 v54, 16, v55
	v_and_b32_e32 v55, 0xffff0000, v55
	v_pk_add_f32 v[44:45], v[44:45], v[64:65]
	v_pk_add_f32 v[46:47], v[46:47], v[54:55]
	v_lshlrev_b32_e32 v54, 16, v50
	v_and_b32_e32 v55, 0xffff0000, v50
	v_lshlrev_b32_e32 v50, 16, v51
	v_and_b32_e32 v51, 0xffff0000, v51
	v_pk_add_f32 v[46:47], v[46:47], v[50:51]
	v_pk_add_f32 v[44:45], v[44:45], v[54:55]
	v_lshlrev_b32_e32 v50, 16, v48
	v_and_b32_e32 v51, 0xffff0000, v48
	v_lshlrev_b32_e32 v48, 16, v49
	v_and_b32_e32 v49, 0xffff0000, v49
	v_pk_add_f32 v[44:45], v[44:45], v[50:51]
	v_pk_add_f32 v[46:47], v[46:47], v[48:49]
	v_lshlrev_b32_e32 v48, 16, v52
	v_and_b32_e32 v49, 0xffff0000, v52
	v_pk_add_f32 v[44:45], v[44:45], v[48:49]
	v_lshlrev_b32_e32 v48, 16, v56
	v_and_b32_e32 v49, 0xffff0000, v56
	v_lshlrev_b32_e32 v50, 16, v53
	v_and_b32_e32 v51, 0xffff0000, v53
	v_pk_add_f32 v[44:45], v[44:45], v[48:49]
	v_lshlrev_b32_e32 v48, 16, v58
	v_and_b32_e32 v49, 0xffff0000, v58
	v_pk_add_f32 v[46:47], v[46:47], v[50:51]
	v_lshlrev_b32_e32 v50, 16, v57
	v_and_b32_e32 v51, 0xffff0000, v57
	v_pk_add_f32 v[44:45], v[44:45], v[48:49]
	v_lshlrev_b32_e32 v48, 16, v60
	v_and_b32_e32 v49, 0xffff0000, v60
	v_pk_add_f32 v[46:47], v[46:47], v[50:51]
	v_lshlrev_b32_e32 v50, 16, v59
	v_and_b32_e32 v51, 0xffff0000, v59
	v_pk_add_f32 v[44:45], v[44:45], v[48:49]
	v_lshlrev_b32_e32 v48, 16, v62
	v_and_b32_e32 v49, 0xffff0000, v62
	v_pk_add_f32 v[46:47], v[46:47], v[50:51]
	v_lshlrev_b32_e32 v50, 16, v61
	v_and_b32_e32 v51, 0xffff0000, v61
	v_pk_add_f32 v[44:45], v[44:45], v[48:49]
	v_lshlrev_b32_e32 v48, 16, v76
	v_and_b32_e32 v49, 0xffff0000, v76
	v_pk_add_f32 v[46:47], v[46:47], v[50:51]
	v_lshlrev_b32_e32 v50, 16, v63
	v_and_b32_e32 v51, 0xffff0000, v63
	v_pk_add_f32 v[44:45], v[44:45], v[48:49]
	v_pk_add_f32 v[46:47], v[46:47], v[50:51]
	v_lshlrev_b32_e32 v50, 16, v77
	v_and_b32_e32 v51, 0xffff0000, v77
	v_pk_add_f32 v[46:47], v[46:47], v[50:51]
	v_and_b32_sdwa v48, v36, v91 dst_sel:DWORD dst_unused:UNUSED_PAD src0_sel:WORD_1 src1_sel:DWORD
	v_add3_u32 v36, v36, v48, s41
	v_and_b32_e32 v32, 0xffff0000, v32
	s_waitcnt vmcnt(3)
	v_pk_fma_f32 v[34:35], v[44:45], v[238:239], v[34:35]
	v_pk_fma_f32 v[38:39], v[46:47], v[240:241], v[38:39]
	v_bfe_u32 v44, v34, 16, 1
	v_add3_u32 v44, v34, v44, s41
	v_bfe_u32 v45, v35, 16, 1
	v_and_b32_sdwa v46, v35, v91 dst_sel:DWORD dst_unused:UNUSED_PAD src0_sel:WORD_1 src1_sel:DWORD
	v_lshrrev_b32_e32 v44, 16, v44
	v_add3_u32 v45, v35, v45, s41
	v_and_b32_sdwa v47, v34, v91 dst_sel:DWORD dst_unused:UNUSED_PAD src0_sel:WORD_1 src1_sel:DWORD
	v_add3_u32 v35, v35, v46, s41
	v_and_b32_sdwa v46, v39, v91 dst_sel:DWORD dst_unused:UNUSED_PAD src0_sel:WORD_1 src1_sel:DWORD
	v_and_or_b32 v44, v45, s3, v44
	v_bfe_u32 v45, v38, 16, 1
	v_add3_u32 v34, v34, v47, s41
	v_and_b32_sdwa v47, v38, v91 dst_sel:DWORD dst_unused:UNUSED_PAD src0_sel:WORD_1 src1_sel:DWORD
	v_add3_u32 v39, v39, v46, s41
	v_add3_u32 v45, v38, v45, s41
	v_add3_u32 v38, v38, v47, s41
	v_and_b32_e32 v39, 0xffff0000, v39
	v_and_b32_e32 v30, 0xffff0000, v30
	v_and_b32_e32 v41, 0xffff0000, v41
	v_and_b32_e32 v40, 0xffff0000, v40
	v_and_b32_e32 v36, 0xffff0000, v36
	v_and_b32_e32 v35, 0xffff0000, v35
	v_and_b32_e32 v34, 0xffff0000, v34
	v_and_b32_e32 v38, 0xffff0000, v38
	v_or_b32_sdwa v45, v39, v45 dst_sel:DWORD dst_unused:UNUSED_PAD src0_sel:DWORD src1_sel:WORD_1
	global_store_dwordx2 v[42:43], v[44:45], off
	s_branch .LBB0_2016

.LBB0_2232:
	v_add_co_u32_e32 v18, vcc, 0xdcc00000, v28
	s_cmpk_lt_i32 s6, 0x400
	s_nop 0
	v_addc_co_u32_e32 v19, vcc, -1, v29, vcc
	global_load_dwordx2 v[20:21], v[18:19], off offset:-1536
	global_load_dwordx2 v[34:35], v[18:19], off offset:-1024
	global_load_dwordx2 v[36:37], v[18:19], off offset:-512
	s_nop 0
	global_load_dwordx2 v[18:19], v[18:19], off
	s_cselect_b64 s[4:5], -1, 0
	s_cmpk_gt_i32 s6, 0x3ff
	s_waitcnt vmcnt(3)
	v_lshlrev_b32_e32 v30, 16, v20
	v_and_b32_e32 v31, 0xffff0000, v20
	v_lshlrev_b32_e32 v32, 16, v21
	v_and_b32_e32 v33, 0xffff0000, v21
	s_waitcnt vmcnt(2)
	v_lshlrev_b32_e32 v38, 16, v34
	v_and_b32_e32 v39, 0xffff0000, v34
	v_lshlrev_b32_e32 v34, 16, v35
	v_and_b32_e32 v35, 0xffff0000, v35
	s_waitcnt vmcnt(1)
	v_lshlrev_b32_e32 v44, 16, v36
	v_and_b32_e32 v45, 0xffff0000, v36
	v_lshlrev_b32_e32 v40, 16, v37
	v_and_b32_e32 v41, 0xffff0000, v37
	s_waitcnt vmcnt(0)
	v_lshlrev_b32_e32 v36, 16, v18
	v_and_b32_e32 v37, 0xffff0000, v18
	v_lshlrev_b32_e32 v42, 16, v19
	v_and_b32_e32 v43, 0xffff0000, v19
	s_cbranch_scc1 .LBB0_2231
	v_add_co_u32_e32 v76, vcc, 0xfec00000, v28
	v_lshl_add_u64 v[46:47], v[28:29], 0, s[14:15]
	s_nop 0
	v_addc_co_u32_e32 v77, vcc, -1, v29, vcc
	v_add_co_u32_e32 v74, vcc, s7, v28
	global_load_dwordx2 v[50:51], v[76:77], off offset:-1536
	s_nop 0
	v_addc_co_u32_e32 v75, vcc, -1, v29, vcc
	v_add_co_u32_e32 v78, vcc, s9, v28
	global_load_dwordx2 v[48:49], v[28:29], off offset:-1536
	s_nop 0
	v_addc_co_u32_e32 v79, vcc, -1, v29, vcc
	v_add_co_u32_e32 v66, vcc, s22, v28
	global_load_dwordx2 v[72:73], v[78:79], off offset:-1536
	global_load_dwordx2 v[52:53], v[74:75], off offset:-1536
	v_addc_co_u32_e32 v67, vcc, -1, v29, vcc
	v_add_co_u32_e32 v62, vcc, s23, v28
	global_load_dwordx2 v[70:71], v[66:67], off offset:-1536
	s_nop 0
	v_addc_co_u32_e32 v63, vcc, -1, v29, vcc
	v_add_co_u32_e32 v56, vcc, s30, v28
	global_load_dwordx2 v[68:69], v[62:63], off offset:-1536
	s_nop 0
	v_addc_co_u32_e32 v57, vcc, -1, v29, vcc
	v_add_co_u32_e32 v54, vcc, s31, v28
	global_load_dwordx2 v[64:65], v[56:57], off offset:-1536
	s_nop 0
	v_addc_co_u32_e32 v55, vcc, -1, v29, vcc
	global_load_dwordx2 v[58:59], v[54:55], off offset:-1536
	v_add_co_u32_e32 v84, vcc, s33, v28
	s_waitcnt vmcnt(7)
	v_lshlrev_b32_e32 v106, 16, v50
	v_addc_co_u32_e32 v85, vcc, -1, v29, vcc
	global_load_dwordx2 v[86:87], v[84:85], off offset:-1536
	global_load_dwordx4 v[18:21], v[26:27], off
	v_add_co_u32_e32 v80, vcc, s36, v28
	v_and_b32_e32 v107, 0xffff0000, v50
	s_nop 0
	v_addc_co_u32_e32 v81, vcc, -1, v29, vcc
	global_load_dwordx2 v[82:83], v[80:81], off offset:-1536
	global_load_dwordx2 v[60:61], v[76:77], off offset:-1024
	global_load_dwordx2 v[88:89], v[76:77], off offset:-512
	s_nop 0
	global_load_dwordx2 v[76:77], v[76:77], off
	v_add_co_u32_e32 v98, vcc, s37, v28
	v_lshlrev_b32_e32 v50, 16, v51
	s_nop 0
	v_addc_co_u32_e32 v99, vcc, -1, v29, vcc
	global_load_dwordx2 v[100:101], v[98:99], off offset:-1536
	global_load_dwordx2 v[102:103], v[74:75], off offset:-1024
	global_load_dwordx2 v[90:91], v[74:75], off offset:-512
	s_nop 0
	global_load_dwordx2 v[74:75], v[74:75], off
	s_nop 0
	global_load_dwordx2 v[104:105], v[78:79], off offset:-1024
	global_load_dwordx2 v[92:93], v[78:79], off offset:-512
	s_nop 0
	global_load_dwordx2 v[78:79], v[78:79], off
	v_and_b32_e32 v51, 0xffff0000, v51
	v_pk_add_f32 v[50:51], v[50:51], 0 op_sel_hi:[1,0]
	v_pk_add_f32 v[106:107], v[106:107], 0 op_sel_hi:[1,0]
	s_waitcnt vmcnt(17)
	v_lshlrev_b32_e32 v108, 16, v52
	v_and_b32_e32 v109, 0xffff0000, v52
	v_lshlrev_b32_e32 v52, 16, v53
	v_and_b32_e32 v53, 0xffff0000, v53
	v_pk_add_f32 v[106:107], v[106:107], v[108:109]
	v_pk_add_f32 v[50:51], v[50:51], v[52:53]
	v_lshlrev_b32_e32 v52, 16, v72
	v_and_b32_e32 v53, 0xffff0000, v72
	v_lshlrev_b32_e32 v72, 16, v73
	v_and_b32_e32 v73, 0xffff0000, v73
	v_pk_add_f32 v[108:109], v[50:51], v[72:73]
	v_pk_add_f32 v[52:53], v[106:107], v[52:53]
	global_load_dwordx2 v[106:107], v[66:67], off offset:-1024
	global_load_dwordx2 v[72:73], v[66:67], off offset:-512
	global_load_dwordx2 v[50:51], v[66:67], off
	s_waitcnt vmcnt(19)
	v_lshlrev_b32_e32 v66, 16, v70
	v_and_b32_e32 v67, 0xffff0000, v70
	v_lshlrev_b32_e32 v70, 16, v71
	v_and_b32_e32 v71, 0xffff0000, v71
	v_pk_add_f32 v[66:67], v[52:53], v[66:67]
	v_pk_add_f32 v[108:109], v[108:109], v[70:71]
	global_load_dwordx2 v[110:111], v[62:63], off offset:-1024
	global_load_dwordx2 v[70:71], v[62:63], off offset:-512
	global_load_dwordx2 v[52:53], v[62:63], off
	s_waitcnt vmcnt(21)
	v_lshlrev_b32_e32 v62, 16, v68
	v_and_b32_e32 v63, 0xffff0000, v68
	v_lshlrev_b32_e32 v68, 16, v69
	v_and_b32_e32 v69, 0xffff0000, v69
	v_pk_add_f32 v[108:109], v[108:109], v[68:69]
	v_pk_add_f32 v[62:63], v[66:67], v[62:63]
	s_waitcnt vmcnt(20)
	v_lshlrev_b32_e32 v66, 16, v64
	v_and_b32_e32 v67, 0xffff0000, v64
	v_lshlrev_b32_e32 v64, 16, v65
	v_and_b32_e32 v65, 0xffff0000, v65
	v_pk_add_f32 v[62:63], v[62:63], v[66:67]
	v_pk_add_f32 v[64:65], v[108:109], v[64:65]
	s_waitcnt vmcnt(19)
	v_lshlrev_b32_e32 v66, 16, v58
	v_and_b32_e32 v67, 0xffff0000, v58
	v_lshlrev_b32_e32 v58, 16, v59
	v_and_b32_e32 v59, 0xffff0000, v59
	global_load_dwordx2 v[112:113], v[56:57], off offset:-1024
	global_load_dwordx2 v[68:69], v[56:57], off offset:-512
	s_nop 0
	global_load_dwordx2 v[56:57], v[56:57], off
	s_nop 0
	global_load_dwordx2 v[108:109], v[54:55], off offset:-1024
	global_load_dwordx2 v[114:115], v[54:55], off offset:-512
	s_nop 0
	global_load_dwordx2 v[54:55], v[54:55], off
	v_pk_add_f32 v[64:65], v[64:65], v[58:59]
	v_pk_add_f32 v[62:63], v[62:63], v[66:67]
	global_load_dwordx2 v[116:117], v[84:85], off offset:-1024
	global_load_dwordx2 v[118:119], v[84:85], off offset:-512
	global_load_dwordx2 v[58:59], v[84:85], off
	v_lshlrev_b32_e32 v124, 16, v48
	v_and_b32_e32 v125, 0xffff0000, v48
	v_lshlrev_b32_e32 v48, 16, v49
	v_and_b32_e32 v49, 0xffff0000, v49
	s_waitcnt vmcnt(27)
	v_lshlrev_b32_e32 v66, 16, v86
	v_and_b32_e32 v67, 0xffff0000, v86
	v_lshlrev_b32_e32 v84, 16, v87
	v_and_b32_e32 v85, 0xffff0000, v87
	v_pk_add_f32 v[66:67], v[62:63], v[66:67]
	v_pk_add_f32 v[64:65], v[64:65], v[84:85]
	global_load_dwordx2 v[84:85], v[80:81], off offset:-1024
	global_load_dwordx2 v[86:87], v[80:81], off offset:-512
	global_load_dwordx2 v[62:63], v[80:81], off
	s_waitcnt vmcnt(28)
	v_lshlrev_b32_e32 v80, 16, v82
	v_and_b32_e32 v81, 0xffff0000, v82
	v_lshlrev_b32_e32 v82, 16, v83
	v_and_b32_e32 v83, 0xffff0000, v83
	v_pk_add_f32 v[82:83], v[64:65], v[82:83]
	v_pk_add_f32 v[66:67], v[66:67], v[80:81]
	global_load_dwordx2 v[80:81], v[98:99], off offset:-1024
	global_load_dwordx2 v[120:121], v[98:99], off offset:-512
	global_load_dwordx2 v[64:65], v[98:99], off
	s_waitcnt vmcnt(27)
	v_lshlrev_b32_e32 v98, 16, v100
	v_and_b32_e32 v99, 0xffff0000, v100
	v_lshlrev_b32_e32 v100, 16, v101
	v_and_b32_e32 v101, 0xffff0000, v101
	v_pk_add_f32 v[98:99], v[66:67], v[98:99]
	v_pk_add_f32 v[82:83], v[82:83], v[100:101]
	global_load_dwordx2 v[100:101], v[28:29], off offset:-1024
	global_load_dwordx2 v[122:123], v[28:29], off offset:-512
	global_load_dwordx2 v[66:67], v[28:29], off
	v_pk_add_f32 v[48:49], v[82:83], v[48:49]
	v_pk_add_f32 v[82:83], v[98:99], v[124:125]
	v_pk_fma_f32 v[32:33], v[48:49], v[20:21], v[32:33]
	v_pk_fma_f32 v[18:19], v[82:83], v[18:19], v[30:31]
	v_lshlrev_b32_e32 v48, 16, v60
	v_bfe_u32 v20, v18, 16, 1
	v_add3_u32 v30, v18, v20, s40
	v_bfe_u32 v18, v19, 16, 1
	v_and_b32_sdwa v20, v33, v97 dst_sel:DWORD dst_unused:UNUSED_PAD src0_sel:WORD_1 src1_sel:DWORD
	v_add3_u32 v18, v19, v18, s40
	v_bfe_u32 v19, v32, 16, 1
	v_add3_u32 v20, v33, v20, s40
	v_and_b32_e32 v31, 0xffff0000, v18
	v_add3_u32 v19, v32, v19, s40
	v_and_b32_e32 v33, 0xffff0000, v20
	v_or_b32_sdwa v18, v31, v30 dst_sel:DWORD dst_unused:UNUSED_PAD src0_sel:DWORD src1_sel:WORD_1
	v_or_b32_sdwa v19, v33, v19 dst_sel:DWORD dst_unused:UNUSED_PAD src0_sel:DWORD src1_sel:WORD_1
	global_load_dwordx4 v[246:249], v[26:27], off offset:1024
	global_load_dwordx4 v[242:245], v[26:27], off offset:2048
	global_load_dwordx4 v[238:241], v[26:27], off offset:3072
	global_store_dwordx2 v[46:47], v[18:19], off
	v_and_b32_e32 v49, 0xffff0000, v60
	v_lshlrev_b32_e32 v60, 16, v61
	v_and_b32_e32 v61, 0xffff0000, v61
	v_pk_add_f32 v[48:49], v[48:49], 0 op_sel_hi:[1,0]
	v_pk_add_f32 v[60:61], v[60:61], 0 op_sel_hi:[1,0]
	s_waitcnt vmcnt(33)
	v_lshlrev_b32_e32 v82, 16, v102
	v_and_b32_e32 v83, 0xffff0000, v102
	v_lshlrev_b32_e32 v98, 16, v103
	v_and_b32_e32 v99, 0xffff0000, v103
	v_pk_add_f32 v[60:61], v[60:61], v[98:99]
	v_pk_add_f32 v[48:49], v[48:49], v[82:83]
	s_waitcnt vmcnt(30)
	v_lshlrev_b32_e32 v82, 16, v104
	v_and_b32_e32 v83, 0xffff0000, v104
	v_lshlrev_b32_e32 v98, 16, v105
	v_and_b32_e32 v99, 0xffff0000, v105
	v_pk_add_f32 v[48:49], v[48:49], v[82:83]
	v_pk_add_f32 v[60:61], v[60:61], v[98:99]
	s_waitcnt vmcnt(27)
	v_lshlrev_b32_e32 v82, 16, v106
	v_and_b32_e32 v83, 0xffff0000, v106
	v_lshlrev_b32_e32 v98, 16, v107
	v_and_b32_e32 v99, 0xffff0000, v107
	v_pk_add_f32 v[60:61], v[60:61], v[98:99]
	v_pk_add_f32 v[48:49], v[48:49], v[82:83]
	s_waitcnt vmcnt(24)
	v_lshlrev_b32_e32 v82, 16, v110
	v_and_b32_e32 v83, 0xffff0000, v110
	v_lshlrev_b32_e32 v98, 16, v111
	v_and_b32_e32 v99, 0xffff0000, v111
	v_pk_add_f32 v[48:49], v[48:49], v[82:83]
	v_pk_add_f32 v[60:61], v[60:61], v[98:99]
	s_waitcnt vmcnt(21)
	v_lshlrev_b32_e32 v82, 16, v112
	v_and_b32_e32 v83, 0xffff0000, v112
	v_lshlrev_b32_e32 v98, 16, v113
	v_and_b32_e32 v99, 0xffff0000, v113
	v_pk_add_f32 v[60:61], v[60:61], v[98:99]
	v_pk_add_f32 v[48:49], v[48:49], v[82:83]
	s_waitcnt vmcnt(18)
	v_lshlrev_b32_e32 v82, 16, v108
	v_and_b32_e32 v83, 0xffff0000, v108
	v_lshlrev_b32_e32 v98, 16, v109
	v_and_b32_e32 v99, 0xffff0000, v109
	v_pk_add_f32 v[48:49], v[48:49], v[82:83]
	v_pk_add_f32 v[60:61], v[60:61], v[98:99]
	s_waitcnt vmcnt(15)
	v_lshlrev_b32_e32 v82, 16, v116
	v_and_b32_e32 v83, 0xffff0000, v116
	v_lshlrev_b32_e32 v98, 16, v117
	v_and_b32_e32 v99, 0xffff0000, v117
	v_pk_add_f32 v[60:61], v[60:61], v[98:99]
	v_pk_add_f32 v[48:49], v[48:49], v[82:83]
	s_waitcnt vmcnt(12)
	v_lshlrev_b32_e32 v82, 16, v84
	v_and_b32_e32 v83, 0xffff0000, v84
	v_lshlrev_b32_e32 v84, 16, v85
	v_and_b32_e32 v85, 0xffff0000, v85
	v_pk_add_f32 v[48:49], v[48:49], v[82:83]
	v_pk_add_f32 v[60:61], v[60:61], v[84:85]
	s_waitcnt vmcnt(9)
	v_lshlrev_b32_e32 v82, 16, v80
	v_and_b32_e32 v83, 0xffff0000, v80
	v_lshlrev_b32_e32 v80, 16, v81
	v_and_b32_e32 v81, 0xffff0000, v81
	v_pk_add_f32 v[60:61], v[60:61], v[80:81]
	v_pk_add_f32 v[48:49], v[48:49], v[82:83]
	s_waitcnt vmcnt(6)
	v_lshlrev_b32_e32 v80, 16, v100
	v_and_b32_e32 v81, 0xffff0000, v100
	v_pk_add_f32 v[48:49], v[48:49], v[80:81]
	v_lshlrev_b32_e32 v82, 16, v101
	v_and_b32_e32 v83, 0xffff0000, v101
	v_pk_add_f32 v[60:61], v[60:61], v[82:83]
	v_lshl_add_u64 v[46:47], v[28:29], 0, s[16:17]
	v_lshlrev_b32_e32 v80, 16, v89
	v_and_b32_e32 v81, 0xffff0000, v89
	v_pk_add_f32 v[80:81], v[80:81], 0 op_sel_hi:[1,0]
	v_lshlrev_b32_e32 v82, 16, v90
	v_and_b32_e32 v83, 0xffff0000, v90
	v_lshlrev_b32_e32 v84, 16, v91
	v_and_b32_e32 v85, 0xffff0000, v91
	v_pk_add_f32 v[80:81], v[80:81], v[84:85]
	v_lshlrev_b32_e32 v84, 16, v93
	v_and_b32_e32 v85, 0xffff0000, v93
	v_pk_add_f32 v[80:81], v[80:81], v[84:85]
	v_and_b32_e32 v30, 0xffff0000, v30
	s_waitcnt vmcnt(3)
	v_pk_fma_f32 v[38:39], v[48:49], v[246:247], v[38:39]
	s_nop 0
	v_pk_fma_f32 v[34:35], v[60:61], v[248:249], v[34:35]
	v_and_b32_sdwa v20, v35, v97 dst_sel:DWORD dst_unused:UNUSED_PAD src0_sel:WORD_1 src1_sel:DWORD
	v_cvt_pk_bf16_f32 v18, v38, v39
	v_bfe_u32 v19, v34, 16, 1
	v_add3_u32 v20, v35, v20, s40
	v_add3_u32 v19, v34, v19, s40
	v_and_b32_e32 v35, 0xffff0000, v20
	v_or_b32_sdwa v19, v35, v19 dst_sel:DWORD dst_unused:UNUSED_PAD src0_sel:DWORD src1_sel:WORD_1
	global_store_dwordx2 v[46:47], v[18:19], off
	v_and_b32_sdwa v60, v32, v97 dst_sel:DWORD dst_unused:UNUSED_PAD src0_sel:WORD_1 src1_sel:DWORD
	v_add3_u32 v32, v32, v60, s40
	v_and_b32_sdwa v60, v39, v97 dst_sel:DWORD dst_unused:UNUSED_PAD src0_sel:WORD_1 src1_sel:DWORD
	v_and_b32_sdwa v61, v38, v97 dst_sel:DWORD dst_unused:UNUSED_PAD src0_sel:WORD_1 src1_sel:DWORD
	v_add3_u32 v39, v39, v60, s40
	v_add3_u32 v38, v38, v61, s40
	v_lshlrev_b32_e32 v60, 16, v88
	v_and_b32_e32 v61, 0xffff0000, v88
	v_pk_add_f32 v[60:61], v[60:61], 0 op_sel_hi:[1,0]
	v_lshl_add_u64 v[46:47], v[28:29], 0, s[18:19]
	v_pk_add_f32 v[60:61], v[60:61], v[82:83]
	v_lshlrev_b32_e32 v82, 16, v92
	v_and_b32_e32 v83, 0xffff0000, v92
	v_pk_add_f32 v[60:61], v[60:61], v[82:83]
	v_lshlrev_b32_e32 v82, 16, v72
	v_and_b32_e32 v83, 0xffff0000, v72
	v_lshlrev_b32_e32 v72, 16, v73
	v_and_b32_e32 v73, 0xffff0000, v73
	v_pk_add_f32 v[72:73], v[80:81], v[72:73]
	v_pk_add_f32 v[60:61], v[60:61], v[82:83]
	v_lshlrev_b32_e32 v80, 16, v70
	v_and_b32_e32 v81, 0xffff0000, v70
	v_lshlrev_b32_e32 v70, 16, v71
	v_and_b32_e32 v71, 0xffff0000, v71
	v_pk_add_f32 v[60:61], v[60:61], v[80:81]
	v_pk_add_f32 v[70:71], v[72:73], v[70:71]
	v_lshlrev_b32_e32 v72, 16, v68
	v_and_b32_e32 v73, 0xffff0000, v68
	v_lshlrev_b32_e32 v68, 16, v69
	v_and_b32_e32 v69, 0xffff0000, v69
	v_pk_add_f32 v[68:69], v[70:71], v[68:69]
	v_pk_add_f32 v[60:61], v[60:61], v[72:73]
	v_lshlrev_b32_e32 v70, 16, v114
	v_and_b32_e32 v71, 0xffff0000, v114
	v_pk_add_f32 v[60:61], v[60:61], v[70:71]
	v_lshlrev_b32_e32 v70, 16, v118
	v_and_b32_e32 v71, 0xffff0000, v118
	v_lshlrev_b32_e32 v72, 16, v115
	v_and_b32_e32 v73, 0xffff0000, v115
	v_pk_add_f32 v[60:61], v[60:61], v[70:71]
	v_lshlrev_b32_e32 v70, 16, v86
	v_and_b32_e32 v71, 0xffff0000, v86
	v_pk_add_f32 v[68:69], v[68:69], v[72:73]
	v_lshlrev_b32_e32 v72, 16, v119
	v_and_b32_e32 v73, 0xffff0000, v119
	v_pk_add_f32 v[60:61], v[60:61], v[70:71]
	v_lshlrev_b32_e32 v70, 16, v120
	v_and_b32_e32 v71, 0xffff0000, v120
	v_pk_add_f32 v[68:69], v[68:69], v[72:73]
	v_lshlrev_b32_e32 v72, 16, v87
	v_and_b32_e32 v73, 0xffff0000, v87
	v_pk_add_f32 v[60:61], v[60:61], v[70:71]
	v_lshlrev_b32_e32 v70, 16, v122
	v_and_b32_e32 v71, 0xffff0000, v122
	v_pk_add_f32 v[68:69], v[68:69], v[72:73]
	v_lshlrev_b32_e32 v72, 16, v121
	v_and_b32_e32 v73, 0xffff0000, v121
	v_pk_add_f32 v[60:61], v[60:61], v[70:71]
	v_pk_add_f32 v[68:69], v[68:69], v[72:73]
	v_lshlrev_b32_e32 v72, 16, v123
	v_and_b32_e32 v73, 0xffff0000, v123
	v_pk_add_f32 v[68:69], v[68:69], v[72:73]
	v_lshlrev_b32_e32 v70, 16, v75
	v_and_b32_e32 v71, 0xffff0000, v75
	v_lshl_add_u64 v[48:49], v[28:29], 0, s[20:21]
	v_and_b32_e32 v32, 0xffff0000, v32
	v_and_b32_e32 v39, 0xffff0000, v39
	v_and_b32_e32 v38, 0xffff0000, v38
	s_waitcnt vmcnt(3)
	v_pk_fma_f32 v[44:45], v[60:61], v[242:243], v[44:45]
	s_nop 0
	v_pk_fma_f32 v[40:41], v[68:69], v[244:245], v[40:41]
	v_and_b32_sdwa v20, v41, v97 dst_sel:DWORD dst_unused:UNUSED_PAD src0_sel:WORD_1 src1_sel:DWORD
	v_cvt_pk_bf16_f32 v18, v44, v45
	v_bfe_u32 v19, v40, 16, 1
	v_add3_u32 v20, v41, v20, s40
	v_add3_u32 v19, v40, v19, s40
	v_and_b32_e32 v41, 0xffff0000, v20
	v_or_b32_sdwa v19, v41, v19 dst_sel:DWORD dst_unused:UNUSED_PAD src0_sel:DWORD src1_sel:WORD_1
	global_store_dwordx2 v[46:47], v[18:19], off
	v_and_b32_sdwa v46, v34, v97 dst_sel:DWORD dst_unused:UNUSED_PAD src0_sel:WORD_1 src1_sel:DWORD
	v_add3_u32 v34, v34, v46, s40
	v_and_b32_sdwa v46, v45, v97 dst_sel:DWORD dst_unused:UNUSED_PAD src0_sel:WORD_1 src1_sel:DWORD
	v_and_b32_sdwa v47, v44, v97 dst_sel:DWORD dst_unused:UNUSED_PAD src0_sel:WORD_1 src1_sel:DWORD
	v_add3_u32 v45, v45, v46, s40
	v_add3_u32 v44, v44, v47, s40
	v_lshlrev_b32_e32 v46, 16, v76
	v_and_b32_e32 v47, 0xffff0000, v76
	v_lshlrev_b32_e32 v60, 16, v77
	v_and_b32_e32 v61, 0xffff0000, v77
	v_pk_add_f32 v[46:47], v[46:47], 0 op_sel_hi:[1,0]
	v_pk_add_f32 v[60:61], v[60:61], 0 op_sel_hi:[1,0]
	v_lshlrev_b32_e32 v68, 16, v74
	v_and_b32_e32 v69, 0xffff0000, v74
	v_pk_add_f32 v[60:61], v[60:61], v[70:71]
	v_pk_add_f32 v[46:47], v[46:47], v[68:69]
	v_lshlrev_b32_e32 v68, 16, v78
	v_and_b32_e32 v69, 0xffff0000, v78
	v_lshlrev_b32_e32 v70, 16, v79
	v_and_b32_e32 v71, 0xffff0000, v79
	v_pk_add_f32 v[46:47], v[46:47], v[68:69]
	v_pk_add_f32 v[60:61], v[60:61], v[70:71]
	v_lshlrev_b32_e32 v68, 16, v50
	v_and_b32_e32 v69, 0xffff0000, v50
	v_lshlrev_b32_e32 v50, 16, v51
	v_and_b32_e32 v51, 0xffff0000, v51
	v_pk_add_f32 v[50:51], v[60:61], v[50:51]
	v_pk_add_f32 v[46:47], v[46:47], v[68:69]
	v_lshlrev_b32_e32 v60, 16, v52
	v_and_b32_e32 v61, 0xffff0000, v52
	v_lshlrev_b32_e32 v52, 16, v53
	v_and_b32_e32 v53, 0xffff0000, v53
	v_pk_add_f32 v[46:47], v[46:47], v[60:61]
	v_pk_add_f32 v[50:51], v[50:51], v[52:53]
	v_lshlrev_b32_e32 v52, 16, v56
	v_and_b32_e32 v53, 0xffff0000, v56
	v_pk_add_f32 v[46:47], v[46:47], v[52:53]
	v_lshlrev_b32_e32 v52, 16, v54
	v_and_b32_e32 v53, 0xffff0000, v54
	v_pk_add_f32 v[46:47], v[46:47], v[52:53]
	v_lshlrev_b32_e32 v52, 16, v58
	v_and_b32_e32 v53, 0xffff0000, v58
	v_lshlrev_b32_e32 v56, 16, v57
	v_and_b32_e32 v57, 0xffff0000, v57
	v_pk_add_f32 v[46:47], v[46:47], v[52:53]
	v_lshlrev_b32_e32 v52, 16, v62
	v_and_b32_e32 v53, 0xffff0000, v62
	v_pk_add_f32 v[50:51], v[50:51], v[56:57]
	v_lshlrev_b32_e32 v54, 16, v55
	v_and_b32_e32 v55, 0xffff0000, v55
	v_pk_add_f32 v[46:47], v[46:47], v[52:53]
	v_lshlrev_b32_e32 v52, 16, v64
	v_and_b32_e32 v53, 0xffff0000, v64
	v_pk_add_f32 v[50:51], v[50:51], v[54:55]
	v_lshlrev_b32_e32 v54, 16, v59
	v_and_b32_e32 v55, 0xffff0000, v59
	v_pk_add_f32 v[46:47], v[46:47], v[52:53]
	v_lshlrev_b32_e32 v52, 16, v66
	v_and_b32_e32 v53, 0xffff0000, v66
	v_pk_add_f32 v[50:51], v[50:51], v[54:55]
	v_lshlrev_b32_e32 v54, 16, v63
	v_and_b32_e32 v55, 0xffff0000, v63
	v_pk_add_f32 v[46:47], v[46:47], v[52:53]
	v_pk_add_f32 v[50:51], v[50:51], v[54:55]
	v_lshlrev_b32_e32 v54, 16, v65
	v_and_b32_e32 v55, 0xffff0000, v65
	v_pk_add_f32 v[50:51], v[50:51], v[54:55]
	v_lshlrev_b32_e32 v54, 16, v67
	v_and_b32_e32 v55, 0xffff0000, v67
	v_pk_add_f32 v[50:51], v[50:51], v[54:55]
	v_and_b32_sdwa v52, v40, v97 dst_sel:DWORD dst_unused:UNUSED_PAD src0_sel:WORD_1 src1_sel:DWORD
	v_add3_u32 v40, v40, v52, s40
	v_and_b32_e32 v34, 0xffff0000, v34
	v_and_b32_e32 v45, 0xffff0000, v45
	v_and_b32_e32 v44, 0xffff0000, v44
	v_and_b32_e32 v40, 0xffff0000, v40
	s_waitcnt vmcnt(3)
	v_pk_fma_f32 v[18:19], v[46:47], v[238:239], v[36:37]
	s_nop 0
	v_pk_fma_f32 v[20:21], v[50:51], v[240:241], v[42:43]
	v_cvt_pk_bf16_f32 v46, v18, v19
	v_bfe_u32 v36, v20, 16, 1
	v_and_b32_sdwa v37, v18, v97 dst_sel:DWORD dst_unused:UNUSED_PAD src0_sel:WORD_1 src1_sel:DWORD
	v_add3_u32 v47, v20, v36, s40
	v_and_b32_sdwa v36, v19, v97 dst_sel:DWORD dst_unused:UNUSED_PAD src0_sel:WORD_1 src1_sel:DWORD
	v_add3_u32 v18, v18, v37, s40
	v_add3_u32 v19, v19, v36, s40
	v_and_b32_e32 v36, 0xffff0000, v18
	v_and_b32_sdwa v18, v21, v97 dst_sel:DWORD dst_unused:UNUSED_PAD src0_sel:WORD_1 src1_sel:DWORD
	v_and_b32_e32 v37, 0xffff0000, v19
	v_and_b32_sdwa v19, v20, v97 dst_sel:DWORD dst_unused:UNUSED_PAD src0_sel:WORD_1 src1_sel:DWORD
	v_add3_u32 v18, v21, v18, s40
	v_add3_u32 v19, v20, v19, s40
	v_and_b32_e32 v43, 0xffff0000, v18
	v_and_b32_e32 v42, 0xffff0000, v19
	v_or_b32_sdwa v47, v43, v47 dst_sel:DWORD dst_unused:UNUSED_PAD src0_sel:DWORD src1_sel:WORD_1
	global_store_dwordx2 v[48:49], v[46:47], off
	s_branch .LBB0_2231
